# speedup vs baseline: 1.0037x; 1.0007x over previous
.LBB3_32:
	v_lshl_add_u32 v0, v120, 5, s22
	v_or_b32_e32 v1, s23, v121
	s_movk_i32 s0, 0x7f
	v_lshl_or_b32 v7, v93, 1, v0
	s_movk_i32 s1, 0x7e
	s_nop 15
	s_nop 15
	v_cmp_eq_u32_e64 s[4:5], s1, v7
	s_nop 7
	v_cmp_gt_u32_e32 vcc, s0, v1
	v_accvgpr_read_b32 v5, a14
	v_cmp_eq_u32_e64 s[0:1], 0, v1
	v_or_b32_e32 v4, v93, v7
	v_cmp_eq_u32_e64 s[2:3], 0, v4
	v_cndmask_b32_e64 v14, v5, 0, s[0:1]
	v_accvgpr_read_b32 v5, a13
	v_cndmask_b32_e64 v22, v5, 0, s[0:1]
	v_accvgpr_read_b32 v5, a12
	v_cndmask_b32_e64 v116, v5, 0, s[0:1]
	v_accvgpr_read_b32 v5, a49
	v_cndmask_b32_e32 v16, 0, v5, vcc
	v_accvgpr_read_b32 v5, a48
	v_cndmask_b32_e32 v28, 0, v5, vcc
	v_accvgpr_read_b32 v5, a30
	v_cndmask_b32_e64 v10, v5, 0, s[0:1]
	v_accvgpr_read_b32 v5, a29
	v_cndmask_b32_e64 v24, v5, 0, s[0:1]
	v_accvgpr_read_b32 v5, a28
	v_cndmask_b32_e64 v42, v5, 0, s[0:1]
	v_accvgpr_read_b32 v5, a57
	v_cndmask_b32_e32 v20, 0, v5, vcc
	v_accvgpr_read_b32 v5, a56
	v_cndmask_b32_e32 v38, 0, v5, vcc
	v_accvgpr_read_b32 v5, a6
	v_cndmask_b32_e64 v15, v5, 0, s[0:1]
	v_accvgpr_read_b32 v5, a5
	v_cndmask_b32_e64 v23, v5, 0, s[0:1]
	v_accvgpr_read_b32 v5, a4
	v_cndmask_b32_e64 v117, v5, 0, s[0:1]
	v_accvgpr_read_b32 v5, a41
	v_cndmask_b32_e32 v17, 0, v5, vcc
	v_accvgpr_read_b32 v5, a40
	v_cndmask_b32_e32 v29, 0, v5, vcc
	v_accvgpr_read_b32 v5, a17
	v_cndmask_b32_e64 v37, v5, 0, s[0:1]
	v_accvgpr_read_b32 v5, a16
	v_cndmask_b32_e64 v47, v5, 0, s[0:1]
	v_accvgpr_read_b32 v5, a52
	v_cndmask_b32_e32 v45, 0, v5, vcc
	v_accvgpr_read_b32 v5, a68
	v_cndmask_b32_e32 v12, 0, v5, vcc
	v_accvgpr_read_b32 v5, a0
	s_or_b64 s[8:9], s[2:3], s[0:1]
	v_cmp_eq_u32_e64 s[6:7], 15, v93
	v_accvgpr_read_b32 v11, a8
	v_cndmask_b32_e64 v112, v5, 0, s[8:9]
	v_accvgpr_read_b32 v4, a67
	v_mov_b32_e32 v5, 0x90
	s_and_b64 s[4:5], s[6:7], s[4:5]
	v_mov_b64_e32 v[40:41], v[16:17]
	v_cndmask_b32_e64 v16, v11, 0, s[2:3]
	v_cndmask_b32_e64 v11, 12, v5, s[6:7]
	v_cndmask_b32_e64 v61, v4, 0, s[4:5]
	v_accvgpr_read_b32 v4, a61
	s_or_b64 s[6:7], s[4:5], s[0:1]
	v_cndmask_b32_e64 v87, v4, 0, s[6:7]
	v_accvgpr_read_b32 v4, a60
	v_cndmask_b32_e64 v86, v4, 0, s[6:7]
	v_accvgpr_read_b32 v4, a65
	v_cndmask_b32_e64 v5, v4, 0, s[4:5]
	v_accvgpr_read_b32 v4, a64
	v_cndmask_b32_e64 v4, v4, 0, s[4:5]
	s_lshl_b32 s14, s18, 2
	v_mov_b64_e32 v[32:33], v[4:5]
	v_lshl_or_b32 v4, v122, 18, s14
	v_mov_b32_e32 v5, 0
	v_mov_b64_e32 v[62:63], v[14:15]
	v_lshl_add_u64 v[14:15], s[12:13], 0, v[4:5]
	v_lshlrev_b32_e32 v4, 7, v1
	v_lshl_add_u64 v[14:15], v[4:5], 2, v[14:15]
	v_lshlrev_b32_e32 v4, 2, v7
	v_mul_u32_u24_e32 v1, 24, v122
	v_lshl_add_u64 v[54:55], v[14:15], 0, v[4:5]
	v_mbcnt_lo_u32_b32 v138, -1, 0
	v_mbcnt_hi_u32_b32 v138, -1, v138
	v_and_b32_e32 v138, 1, v138
	v_mul_u32_u24_e32 v138, 0xfff8, v138
	v_add_u32_e32 v138, 0xffff0000, v138
	v_mov_b32_e32 v139, -1
	s_mov_b32 s28, 0x55555555
	s_mov_b32 s29, 0x55555555
	s_mov_b32 s30, 0xaaaaaaaa
	s_mov_b32 s31, 0xaaaaaaaa
	v_or_b32_e32 v1, v1, v121
	v_lshlrev_b32_e32 v4, 7, v120
	s_movk_i32 s12, 0x120
	v_mad_u32_u24 v1, v1, s12, v4
	s_add_u32 s12, s10, 0x800000
	v_accvgpr_read_b32 v7, a72
	v_mov_b64_e32 v[80:81], v[28:29]
	s_addc_u32 s13, s11, 0
	v_lshlrev_b64 v[28:29], 2, v[94:95]
	v_readfirstlane_b32 s14, v7
	v_add_u32_e32 v7, 0, v90
	v_lshl_add_u64 v[4:5], s[12:13], 0, v[28:29]
	s_mov_b32 m0, s14
	v_lshlrev_b64 v[30:31], 2, v[96:97]
	v_readfirstlane_b32 s14, v7
	v_mov_b32_e32 v14, v7
	v_add_u32_e32 v7, 0, v91
	s_waitcnt lgkmcnt(0)
	s_barrier
	s_add_u32 s52, s10, 0x1000000
	s_addc_u32 s53, s11, 0
	v_add_u32_e32 v148, 0xe000, v118
	v_lshlrev_b32_e32 v149, 2, v94
	s_nop 0
	v_readfirstlane_b32 s44, v148
	s_mov_b32 m0, s44
	s_nop 0
	global_load_lds_dwordx4 v149, s[52:53] nt
	v_add_u32_e32 v148, 0xe000, v90
	v_lshlrev_b32_e32 v149, 2, v96
	s_nop 0
	v_readfirstlane_b32 s44, v148
	s_mov_b32 m0, s44
	s_nop 0
	global_load_lds_dwordx4 v149, s[52:53] nt
	v_add_u32_e32 v148, 0xe000, v91
	v_lshlrev_b32_e32 v149, 2, v98
	s_nop 0
	v_readfirstlane_b32 s44, v148
	s_mov_b32 m0, s44
	s_nop 0
	global_load_lds_dwordx4 v149, s[52:53] nt
	v_add_u32_e32 v148, 0xe000, v119
	v_lshlrev_b32_e32 v149, 2, v100
	s_nop 0
	v_readfirstlane_b32 s44, v148
	s_mov_b32 m0, s44
	s_nop 0
	global_load_lds_dwordx4 v149, s[52:53] nt
	v_mbcnt_lo_u32_b32 v150, -1, 0
	v_mbcnt_hi_u32_b32 v150, -1, v150
	v_lshlrev_b32_e32 v150, 4, v150
	v_add_u32_e32 v151, v91, v150
	v_add_u32_e32 v152, v119, v150
	v_add_u32_e32 v153, v118, v150
	v_add_u32_e32 v154, v90, v150
	ds_write_b128 v151, v[128:131]
	ds_write_b128 v152, v[132:135]
	ds_write_b128 v153, v[172:175] offset:28672
	ds_write_b128 v154, v[176:179] offset:28672
	ds_write_b128 v151, v[140:143] offset:28672
	ds_write_b128 v152, v[144:147] offset:28672
	v_lshl_add_u64 v[134:135], v[54:55], 0, v[138:139]
	v_lshlrev_b64 v[56:57], 2, v[98:99]
	v_mov_b32_e32 v19, v7
	v_lshlrev_b64 v[58:59], 2, v[100:101]
	v_add_u32_e32 v7, 0, v119
	v_accvgpr_read_b32 v25, a72
	v_mov_b32_e32 v21, v7
	v_lshl_add_u32 v15, v93, 3, v1
	v_add_u32_e32 v1, v1, v11
	s_waitcnt vmcnt(16)
	v_accvgpr_write_b32 a12, v14
	v_mov_b64_e32 v[124:125], v[56:57]
	v_accvgpr_write_b32 a13, v19
	v_mov_b64_e32 v[126:127], v[58:59]
	v_accvgpr_write_b32 a16, v21
	s_waitcnt lgkmcnt(0)
	s_barrier
	v_add_u32_e32 v14, 0x16010, v15
	v_mov_b32_e32 v122, v15
	v_add_u32_e32 v15, 0x16000, v1
	ds_read_b64 v[64:65], v14
	ds_read_b64 v[66:67], v14 offset:288
	ds_read_b64 v[68:69], v14 offset:576
	ds_read_b64 v[76:77], v14 offset:1728
	ds_read_b64 v[78:79], v14 offset:2016
	ds_read_b64 v[4:5], v14 offset:2304
	ds_read_b64 v[84:85], v14 offset:3456
	ds_read_b64 v[74:75], v14 offset:3744
	ds_read_b64 v[88:89], v14 offset:4032
	ds_read_b64 v[100:101], v14 offset:5184
	ds_read_b64 v[106:107], v14 offset:5472
	ds_read_b64 v[120:121], v14 offset:5760
	ds_read_b32 v43, v15
	ds_read_b32 v19, v15 offset:288
	ds_read_b32 v39, v15 offset:576
	ds_read_b32 v25, v15 offset:1728
	ds_read_b32 v7, v15 offset:2016
	ds_read_b32 v21, v15 offset:2304
	ds_read_b32 v11, v15 offset:3456
	ds_read_b32 v35, v15 offset:3744
	ds_read_b32 v59, v15 offset:4032
	ds_read_b32 v57, v15 offset:5184
	ds_read_b32 v51, v15 offset:5472
	ds_read_b32 v49, v15 offset:5760
	s_waitcnt lgkmcnt(0)
	v_accvgpr_read_b32 v8, a26
	v_mov_b32_e32 v46, v43
	v_mov_b32_e32 v113, v65
	v_mov_b32_e32 v26, v19
	v_mov_b32_dpp v46, v65 row_shr:1 row_mask:0xf bank_mask:0xf
	v_pk_mul_f32 v[70:71], v[112:113], v[46:47]
	v_accvgpr_read_b32 v9, a22
	v_accvgpr_read_b32 v27, a36
	v_mov_b32_dpp v43, v64 row_shl:1 row_mask:0xf bank_mask:0xf
	v_mov_b32_dpp v26, v67 row_shr:1 row_mask:0xf bank_mask:0xf
	v_pk_fma_f32 v[70:71], v[64:65], v[116:117], v[70:71] op_sel_hi:[0,1,1]
	v_pk_mov_b32 v[64:65], v[64:65], v[86:87] op_sel:[1,0]
	v_mov_b32_e32 v17, v67
	v_mov_b64_e32 v[102:103], v[8:9]
	v_accvgpr_read_b32 v8, a25
	v_accvgpr_read_b32 v114, a24
	v_accvgpr_read_b32 v9, a21
	v_accvgpr_read_b32 v115, a20
	v_accvgpr_read_b32 v2, a32
	v_mov_b64_e32 v[82:83], v[30:31]
	v_pk_fma_f32 v[70:71], v[64:65], v[42:43], v[70:71]
	v_pk_mul_f32 v[64:65], v[16:17], v[26:27]
	v_mov_b64_e32 v[30:31], v[32:33]
	v_accvgpr_read_b32 v18, a44
	v_mov_b64_e32 v[104:105], v[8:9]
	v_cndmask_b32_e32 v9, 0, v2, vcc
	v_accvgpr_write_b32 a4, v14
	v_mov_b32_dpp v19, v66 row_shl:1 row_mask:0xf bank_mask:0xf
	v_pk_fma_f32 v[64:65], v[66:67], v[114:115], v[64:65] op_sel_hi:[0,1,1]
	v_pk_mov_b32 v[66:67], v[66:67], v[30:31] op_sel:[1,0]
	v_accvgpr_read_b32 v14, a69
	v_mov_b32_e32 v44, v39
	v_mov_b32_e32 v60, v1
	v_pk_fma_f32 v[66:67], v[66:67], v[18:19], v[64:65]
	v_cndmask_b32_e32 v14, 0, v14, vcc
	v_cndmask_b32_e64 v0, v9, 0, s[2:3]
	v_mov_b32_dpp v44, v69 row_shr:1 row_mask:0xf bank_mask:0xf
	v_pk_add_f32 v[70:71], v[70:71], 0 op_sel_hi:[1,0]
	v_mov_b32_e32 v1, v69
	v_accvgpr_write_b32 a0, v15
	v_cndmask_b32_e64 v15, v14, 0, s[4:5]
	v_cndmask_b32_e64 v14, v12, 0, s[4:5]
	v_pk_add_f32 v[66:67], v[70:71], v[66:67]
	v_pk_mul_f32 v[70:71], v[0:1], v[44:45]
	v_mov_b32_dpp v39, v68 row_shl:1 row_mask:0xf bank_mask:0xf
	v_pk_fma_f32 v[70:71], v[68:69], v[80:81], v[70:71] op_sel_hi:[0,1,1]
	v_pk_mov_b32 v[68:69], v[68:69], v[14:15] op_sel:[1,0]
	v_accvgpr_read_b32 v9, a1
	v_pk_fma_f32 v[68:69], v[68:69], v[38:39], v[70:71]
	v_mov_b32_e32 v36, v25
	v_cndmask_b32_e64 v64, v9, 0, s[8:9]
	v_pk_add_f32 v[66:67], v[66:67], v[68:69]
	v_mov_b32_dpp v36, v77 row_shr:1 row_mask:0xf bank_mask:0xf
	v_mov_b32_e32 v65, v77
	v_mov_b64_e32 v[108:109], v[22:23]
	v_accvgpr_read_b32 v9, a9
	v_mov_b32_e32 v128, v66
	v_mov_b32_e32 v129, v67
	v_mov_b32_e32 v12, v7
	v_pk_mul_f32 v[66:67], v[64:65], v[36:37]
	v_accvgpr_read_b32 v13, a37
	v_mov_b64_e32 v[72:73], v[28:29]
	v_cndmask_b32_e64 v28, v9, 0, s[2:3]
	v_mov_b32_dpp v25, v76 row_shl:1 row_mask:0xf bank_mask:0xf
	v_mov_b32_dpp v12, v79 row_shr:1 row_mask:0xf bank_mask:0xf
	v_pk_fma_f32 v[66:67], v[76:77], v[108:109], v[66:67] op_sel_hi:[0,1,1]
	v_mov_b32_e32 v76, v77
	v_mov_b32_e32 v77, v87
	v_mov_b32_e32 v29, v79
	v_pk_fma_f32 v[66:67], v[76:77], v[24:25], v[66:67]
	v_pk_mul_f32 v[76:77], v[28:29], v[12:13]
	v_accvgpr_read_b32 v6, a45
	v_accvgpr_read_b32 v2, a33
	v_mov_b32_dpp v7, v78 row_shl:1 row_mask:0xf bank_mask:0xf
	v_pk_fma_f32 v[76:77], v[78:79], v[104:105], v[76:77] op_sel_hi:[0,1,1]
	v_mov_b32_e32 v78, v79
	v_mov_b32_e32 v79, v31
	v_cndmask_b32_e32 v2, 0, v2, vcc
	v_accvgpr_read_b32 v50, a53
	v_pk_fma_f32 v[76:77], v[78:79], v[6:7], v[76:77]
	v_mov_b32_e32 v78, v21
	v_accvgpr_write_b32 a44, v80
	v_cndmask_b32_e32 v79, 0, v50, vcc
	v_cndmask_b32_e64 v52, v2, 0, s[2:3]
	v_mov_b32_dpp v78, v5 row_shr:1 row_mask:0xf bank_mask:0xf
	v_pk_add_f32 v[66:67], v[66:67], 0 op_sel_hi:[1,0]
	v_mov_b32_e32 v53, v5
	v_accvgpr_write_b32 a45, v81
	v_accvgpr_write_b32 a21, v15
	v_pk_add_f32 v[80:81], v[66:67], v[76:77]
	v_pk_mul_f32 v[66:67], v[52:53], v[78:79]
	v_accvgpr_write_b32 a24, v40
	v_accvgpr_read_b32 v2, a2
	v_mov_b32_dpp v21, v4 row_shl:1 row_mask:0xf bank_mask:0xf
	v_pk_fma_f32 v[66:67], v[4:5], v[40:41], v[66:67] op_sel_hi:[0,1,1]
	v_accvgpr_write_b32 a25, v41
	v_mov_b32_e32 v4, v5
	v_accvgpr_read_b32 v5, a21
	v_cndmask_b32_e64 v40, v2, 0, s[8:9]
	v_accvgpr_read_b32 v2, a62
	v_accvgpr_read_b32 v8, a18
	v_accvgpr_read_b32 v48, a63
	v_accvgpr_write_b32 a20, v14
	v_accvgpr_write_b32 a41, v23
	v_pk_fma_f32 v[4:5], v[4:5], v[20:21], v[66:67]
	s_mov_b64 s[12:13], 0x10000
	v_cndmask_b32_e64 v14, v2, 0, s[6:7]
	v_mov_b32_e32 v76, v11
	v_accvgpr_read_b32 v2, a10
	v_accvgpr_write_b32 a40, v22
	v_cndmask_b32_e64 v15, v48, 0, s[6:7]
	v_cndmask_b32_e64 v77, v8, 0, s[0:1]
	v_pk_add_f32 v[4:5], v[80:81], v[4:5]
	v_lshl_add_u64 v[136:137], v[134:135], 0, s[12:13]
	v_mov_b32_dpp v76, v85 row_shr:1 row_mask:0xf bank_mask:0xf
	v_mov_b32_e32 v41, v85
	v_cndmask_b32_e64 v22, v2, 0, s[2:3]
	v_mov_b32_e32 v2, v35
	v_accvgpr_read_b32 v1, a50
	v_accvgpr_read_b32 v3, a38
	s_mov_b64 s[32:33], vcc
	s_nop 1
	s_mov_b64 vcc, s[28:29]
	s_nop 0
	v_cndmask_b32_dpp v130, v4, v128, vcc quad_perm:[1,0,3,2] row_mask:0xf bank_mask:0xf
	v_cndmask_b32_dpp v131, v5, v129, vcc quad_perm:[1,0,3,2] row_mask:0xf bank_mask:0xf
	s_mov_b64 vcc, s[30:31]
	s_nop 0
	v_cndmask_b32_dpp v132, v128, v4, vcc quad_perm:[1,0,3,2] row_mask:0xf bank_mask:0xf
	v_cndmask_b32_dpp v133, v129, v5, vcc quad_perm:[1,0,3,2] row_mask:0xf bank_mask:0xf
	global_store_dwordx4 v[136:137], v[130:133], off sc0 sc1 nt
	s_nop 1
	s_mov_b64 vcc, s[32:33]
	v_mov_b64_e32 v[8:9], v[14:15]
	v_pk_mul_f32 v[4:5], v[40:41], v[76:77]
	v_mov_b64_e32 v[66:67], v[62:63]
	v_mov_b32_dpp v2, v75 row_shr:1 row_mask:0xf bank_mask:0xf
	v_mov_b32_e32 v23, v75
	v_cndmask_b32_e32 v62, 0, v1, vcc
	v_accvgpr_read_b32 v1, a42
	v_mov_b32_dpp v11, v84 row_shl:1 row_mask:0xf bank_mask:0xf
	v_pk_fma_f32 v[4:5], v[84:85], v[66:67], v[4:5] op_sel_hi:[0,1,1]
	v_pk_mov_b32 v[80:81], v[84:85], v[8:9] op_sel:[1,0]
	v_pk_mul_f32 v[84:85], v[22:23], v[2:3]
	v_accvgpr_read_b32 v2, a58
	v_cndmask_b32_e32 v63, 0, v1, vcc
	v_accvgpr_read_b32 v1, a70
	v_pk_fma_f32 v[80:81], v[80:81], v[10:11], v[4:5]
	v_accvgpr_read_b32 v4, a66
	v_cndmask_b32_e32 v58, 0, v2, vcc
	v_cndmask_b32_e32 v1, 0, v1, vcc
	v_accvgpr_read_b32 v2, a71
	v_cndmask_b32_e64 v8, v4, 0, s[4:5]
	v_cndmask_b32_e32 v2, 0, v2, vcc
	v_cndmask_b32_e64 v4, v1, 0, s[4:5]
	v_accvgpr_read_b32 v1, a34
	v_mov_b32_e32 v9, v61
	v_cndmask_b32_e64 v5, v2, 0, s[4:5]
	v_cndmask_b32_e32 v1, 0, v1, vcc
	v_accvgpr_read_b32 v2, a54
	v_mov_b32_e32 v92, v59
	v_accvgpr_read_b32 v34, a46
	v_mov_b32_dpp v35, v74 row_shl:1 row_mask:0xf bank_mask:0xf
	v_pk_fma_f32 v[84:85], v[74:75], v[102:103], v[84:85] op_sel_hi:[0,1,1]
	v_pk_mov_b32 v[74:75], v[74:75], v[8:9] op_sel:[1,0]
	v_cndmask_b32_e32 v93, 0, v2, vcc
	v_mov_b32_dpp v92, v89 row_shr:1 row_mask:0xf bank_mask:0xf
	v_cndmask_b32_e64 v96, v1, 0, s[2:3]
	v_mov_b32_e32 v97, v89
	v_accvgpr_read_b32 v1, a31
	v_pk_fma_f32 v[74:75], v[74:75], v[34:35], v[84:85]
	v_pk_mul_f32 v[84:85], v[96:97], v[92:93]
	v_accvgpr_write_b32 a8, v62
	v_cndmask_b32_e64 v56, v1, 0, s[0:1]
	v_accvgpr_read_b32 v1, a15
	v_pk_fma_f32 v[84:85], v[88:89], v[62:63], v[84:85] op_sel_hi:[0,1,1]
	v_accvgpr_write_b32 a9, v63
	v_cndmask_b32_e64 v62, v1, 0, s[0:1]
	v_accvgpr_read_b32 v1, a7
	v_cndmask_b32_e64 v63, v1, 0, s[0:1]
	v_accvgpr_read_b32 v1, a19
	v_pk_add_f32 v[80:81], v[80:81], 0 op_sel_hi:[1,0]
	v_mov_b32_dpp v59, v88 row_shl:1 row_mask:0xf bank_mask:0xf
	v_pk_mov_b32 v[88:89], v[88:89], v[4:5] op_sel:[1,0]
	v_cndmask_b32_e64 v95, v1, 0, s[0:1]
	v_accvgpr_read_b32 v1, a3
	v_accvgpr_write_b32 a36, v104
	v_pk_add_f32 v[80:81], v[80:81], v[74:75]
	v_pk_fma_f32 v[84:85], v[88:89], v[58:59], v[84:85]
	v_mov_b32_e32 v94, v57
	v_cndmask_b32_e64 v98, v1, 0, s[8:9]
	v_accvgpr_read_b32 v1, a11
	v_accvgpr_write_b32 a37, v105
	v_accvgpr_write_b32 a32, v102
	v_pk_add_f32 v[80:81], v[80:81], v[84:85]
	s_mov_b64 s[4:5], 0x20000
	v_mov_b32_dpp v94, v101 row_shr:1 row_mask:0xf bank_mask:0xf
	v_mov_b32_e32 v99, v101
	v_cndmask_b32_e64 v104, v1, 0, s[2:3]
	v_accvgpr_read_b32 v1, a59
	v_accvgpr_write_b32 a29, v15
	v_accvgpr_write_b32 a33, v103
	v_accvgpr_write_b32 a49, v5
	v_lshl_add_u64 v[84:85], v[54:55], 0, s[4:5]
	v_mov_b32_e32 v128, v80
	v_mov_b32_e32 v129, v81
	v_pk_mul_f32 v[80:81], v[98:99], v[94:95]
	v_mov_b32_e32 v102, v51
	v_cndmask_b32_e32 v48, 0, v1, vcc
	v_accvgpr_read_b32 v1, a51
	v_accvgpr_write_b32 a48, v4
	v_mov_b32_dpp v57, v100 row_shl:1 row_mask:0xf bank_mask:0xf
	v_pk_fma_f32 v[80:81], v[100:101], v[62:63], v[80:81] op_sel_hi:[0,1,1]
	v_mov_b32_e32 v84, v101
	v_accvgpr_read_b32 v85, a29
	v_accvgpr_read_b32 v103, a39
	v_mov_b32_dpp v102, v107 row_shr:1 row_mask:0xf bank_mask:0xf
	v_mov_b32_e32 v105, v107
	v_cndmask_b32_e32 v4, 0, v1, vcc
	v_accvgpr_read_b32 v1, a43
	v_pk_fma_f32 v[80:81], v[84:85], v[56:57], v[80:81]
	v_accvgpr_read_b32 v30, a27
	v_accvgpr_read_b32 v31, a23
	v_pk_mul_f32 v[84:85], v[104:105], v[102:103]
	v_cndmask_b32_e32 v5, 0, v1, vcc
	v_accvgpr_read_b32 v1, a35
	v_accvgpr_read_b32 v50, a47
	v_mov_b32_dpp v51, v106 row_shl:1 row_mask:0xf bank_mask:0xf
	v_pk_fma_f32 v[84:85], v[106:107], v[30:31], v[84:85] op_sel_hi:[0,1,1]
	v_mov_b32_e32 v106, v107
	v_mov_b32_e32 v107, v9
	v_cndmask_b32_e32 v1, 0, v1, vcc
	v_accvgpr_read_b32 v2, a55
	v_mov_b32_e32 v108, v49
	v_pk_fma_f32 v[84:85], v[106:107], v[50:51], v[84:85]
	v_pk_add_f32 v[80:81], v[80:81], 0 op_sel_hi:[1,0]
	v_cndmask_b32_e32 v109, 0, v2, vcc
	v_mov_b32_dpp v108, v121 row_shr:1 row_mask:0xf bank_mask:0xf
	v_cndmask_b32_e64 v110, v1, 0, s[2:3]
	v_mov_b32_e32 v111, v121
	v_pk_add_f32 v[80:81], v[80:81], v[84:85]
	v_pk_mul_f32 v[84:85], v[110:111], v[108:109]
	v_mov_b32_dpp v49, v120 row_shl:1 row_mask:0xf bank_mask:0xf
	v_pk_fma_f32 v[84:85], v[120:121], v[4:5], v[84:85] op_sel_hi:[0,1,1]
	v_mov_b32_e32 v120, v121
	v_accvgpr_read_b32 v121, a49
	v_pk_fma_f32 v[84:85], v[120:121], v[48:49], v[84:85]
	s_mov_b64 s[0:1], 0x30000
	v_pk_add_f32 v[80:81], v[80:81], v[84:85]
	v_lshl_add_u64 v[136:137], v[134:135], 0, s[0:1]
	v_add_u32_e32 v1, s17, v118
	s_add_u32 s0, s10, 0x1400000
	s_mov_b64 s[32:33], vcc
	s_nop 1
	s_mov_b64 vcc, s[28:29]
	s_nop 0
	v_cndmask_b32_dpp v130, v80, v128, vcc quad_perm:[1,0,3,2] row_mask:0xf bank_mask:0xf
	v_cndmask_b32_dpp v131, v81, v129, vcc quad_perm:[1,0,3,2] row_mask:0xf bank_mask:0xf
	s_mov_b64 vcc, s[30:31]
	s_nop 0
	v_cndmask_b32_dpp v132, v128, v80, vcc quad_perm:[1,0,3,2] row_mask:0xf bank_mask:0xf
	v_cndmask_b32_dpp v133, v129, v81, vcc quad_perm:[1,0,3,2] row_mask:0xf bank_mask:0xf
	global_store_dwordx4 v[136:137], v[130:133], off sc0 sc1 nt
	s_nop 1
	s_mov_b64 vcc, s[32:33]
	v_readfirstlane_b32 s2, v1
	s_addc_u32 s1, s11, 0
	v_add_u32_e32 v1, s17, v90
	s_waitcnt vmcnt(6)
	v_lshl_add_u64 v[80:81], s[0:1], 0, v[72:73]
	s_mov_b32 m0, s2
	v_readfirstlane_b32 s2, v1
	v_mov_b64_e32 v[74:75], v[82:83]
	v_add_u32_e32 v1, s17, v91
	s_waitcnt lgkmcnt(0)
	s_barrier
	global_load_lds_dwordx4 v[80:81], off nt
	v_lshl_add_u64 v[80:81], s[0:1], 0, v[74:75]
	s_mov_b32 m0, s2
	v_readfirstlane_b32 s2, v1
	v_add_u32_e32 v1, s17, v119
	global_load_lds_dwordx4 v[80:81], off nt
	v_lshl_add_u64 v[80:81], s[0:1], 0, v[124:125]
	s_mov_b32 m0, s2
	v_readfirstlane_b32 s2, v1
	global_load_lds_dwordx4 v[80:81], off nt
	v_lshl_add_u64 v[80:81], s[0:1], 0, v[126:127]
	s_mov_b32 m0, s2
	v_accvgpr_write_b32 a53, v33
	v_accvgpr_write_b32 a2, v62
	v_accvgpr_write_b32 a7, v5
	v_accvgpr_write_b32 a22, v124
	v_accvgpr_write_b32 a30, v126
	global_load_lds_dwordx4 v[80:81], off nt
	v_accvgpr_write_b32 a52, v32
	v_accvgpr_write_b32 a3, v63
	v_accvgpr_write_b32 a6, v4
	v_mov_b64_e32 v[32:33], v[72:73]
	v_accvgpr_write_b32 a23, v125
	v_accvgpr_write_b32 a31, v127
	v_add_u32_e32 v2, 0x1d010, v122
	v_accvgpr_write_b32 a10, v122
	v_add_u32_e32 v5, 0x1d000, v60
	v_mov_b32_e32 v4, v60
	ds_read_b64 v[62:63], v2
	ds_read_b64 v[60:61], v2 offset:288
	ds_read_b64 v[72:73], v2 offset:576
	ds_read_b64 v[70:71], v2 offset:1728
	ds_read_b64 v[68:69], v2 offset:2016
	ds_read_b64 v[82:83], v2 offset:2304
	ds_read_b64 v[80:81], v2 offset:3456
	ds_read_b64 v[84:85], v2 offset:3744
	ds_read_b64 v[126:127], v2 offset:4032
	ds_read_b64 v[124:125], v2 offset:5184
	ds_read_b64 v[122:123], v2 offset:5472
	ds_read_b64 v[120:121], v2 offset:5760
	ds_read_b32 v43, v5
	ds_read_b32 v19, v5 offset:288
	ds_read_b32 v39, v5 offset:576
	ds_read_b32 v25, v5 offset:1728
	ds_read_b32 v7, v5 offset:2016
	ds_read_b32 v21, v5 offset:2304
	ds_read_b32 v11, v5 offset:3456
	ds_read_b32 v35, v5 offset:3744
	ds_read_b32 v59, v5 offset:4032
	ds_read_b32 v57, v5 offset:5184
	ds_read_b32 v51, v5 offset:5472
	ds_read_b32 v49, v5 offset:5760
	s_waitcnt lgkmcnt(0)
	v_mov_b64_e32 v[100:101], v[86:87]
	v_mov_b32_e32 v46, v43
	v_mov_b32_e32 v113, v63
	v_mov_b32_e32 v26, v19
	v_mov_b32_dpp v46, v63 row_shr:1 row_mask:0xf bank_mask:0xf
	v_pk_mul_f32 v[88:89], v[112:113], v[46:47]
	v_mov_b32_dpp v43, v62 row_shl:1 row_mask:0xf bank_mask:0xf
	v_pk_fma_f32 v[88:89], v[62:63], v[116:117], v[88:89] op_sel_hi:[0,1,1]
	v_pk_mov_b32 v[62:63], v[62:63], v[100:101] op_sel:[1,0]
	v_mov_b32_dpp v26, v61 row_shr:1 row_mask:0xf bank_mask:0xf
	v_mov_b32_e32 v17, v61
	v_pk_fma_f32 v[62:63], v[62:63], v[42:43], v[88:89]
	v_pk_mul_f32 v[88:89], v[16:17], v[26:27]
	v_accvgpr_write_b32 a34, v16
	v_accvgpr_read_b32 v16, a52
	v_accvgpr_read_b32 v17, a53
	v_mov_b32_dpp v19, v60 row_shl:1 row_mask:0xf bank_mask:0xf
	v_pk_fma_f32 v[88:89], v[60:61], v[114:115], v[88:89] op_sel_hi:[0,1,1]
	v_pk_mov_b32 v[60:61], v[60:61], v[16:17] op_sel:[1,0]
	v_mov_b32_e32 v44, v39
	v_accvgpr_write_b32 a28, v14
	v_pk_fma_f32 v[60:61], v[60:61], v[18:19], v[88:89]
	v_pk_add_f32 v[62:63], v[62:63], 0 op_sel_hi:[1,0]
	v_mov_b32_dpp v44, v73 row_shr:1 row_mask:0xf bank_mask:0xf
	v_mov_b32_e32 v1, v73
	v_accvgpr_read_b32 v14, a44
	v_accvgpr_read_b32 v89, a21
	v_pk_add_f32 v[60:61], v[62:63], v[60:61]
	v_pk_mul_f32 v[62:63], v[0:1], v[44:45]
	v_accvgpr_read_b32 v15, a45
	v_accvgpr_read_b32 v88, a20
	v_mov_b32_dpp v39, v72 row_shl:1 row_mask:0xf bank_mask:0xf
	v_pk_fma_f32 v[62:63], v[72:73], v[14:15], v[62:63] op_sel_hi:[0,1,1]
	v_pk_mov_b32 v[72:73], v[72:73], v[88:89] op_sel:[1,0]
	v_mov_b32_e32 v36, v25
	v_pk_fma_f32 v[62:63], v[72:73], v[38:39], v[62:63]
	s_mov_b64 s[0:1], 0x400000
	v_pk_add_f32 v[60:61], v[60:61], v[62:63]
	v_mov_b32_dpp v36, v71 row_shr:1 row_mask:0xf bank_mask:0xf
	v_mov_b32_e32 v65, v71
	v_accvgpr_read_b32 v87, a41
	v_lshl_add_u64 v[62:63], v[54:55], 0, s[0:1]
	v_mov_b32_e32 v128, v60
	v_mov_b32_e32 v129, v61
	v_pk_mul_f32 v[60:61], v[64:65], v[36:37]
	v_accvgpr_read_b32 v86, a40
	v_mov_b32_e32 v12, v7
	v_mov_b32_dpp v25, v70 row_shl:1 row_mask:0xf bank_mask:0xf
	v_pk_fma_f32 v[60:61], v[70:71], v[86:87], v[60:61] op_sel_hi:[0,1,1]
	v_mov_b32_e32 v62, v71
	v_mov_b32_e32 v63, v101
	v_mov_b32_dpp v12, v69 row_shr:1 row_mask:0xf bank_mask:0xf
	v_mov_b32_e32 v29, v69
	v_accvgpr_read_b32 v107, a37
	v_pk_fma_f32 v[60:61], v[62:63], v[24:25], v[60:61]
	v_pk_mul_f32 v[62:63], v[28:29], v[12:13]
	v_accvgpr_read_b32 v106, a36
	v_mov_b32_dpp v7, v68 row_shl:1 row_mask:0xf bank_mask:0xf
	v_pk_fma_f32 v[62:63], v[68:69], v[106:107], v[62:63] op_sel_hi:[0,1,1]
	v_mov_b32_e32 v68, v69
	v_mov_b32_e32 v69, v17
	v_mov_b32_e32 v78, v21
	v_pk_fma_f32 v[62:63], v[68:69], v[6:7], v[62:63]
	v_pk_add_f32 v[60:61], v[60:61], 0 op_sel_hi:[1,0]
	v_mov_b32_dpp v78, v83 row_shr:1 row_mask:0xf bank_mask:0xf
	v_mov_b32_e32 v53, v83
	v_accvgpr_read_b32 v14, a24
	v_pk_add_f32 v[60:61], v[60:61], v[62:63]
	v_pk_mul_f32 v[62:63], v[52:53], v[78:79]
	v_accvgpr_read_b32 v15, a25
	v_mov_b32_dpp v21, v82 row_shl:1 row_mask:0xf bank_mask:0xf
	v_pk_fma_f32 v[62:63], v[82:83], v[14:15], v[62:63] op_sel_hi:[0,1,1]
	v_mov_b32_e32 v68, v83
	v_mov_b32_e32 v69, v89
	v_pk_fma_f32 v[62:63], v[68:69], v[20:21], v[62:63]
	v_mov_b32_e32 v76, v11
	v_pk_add_f32 v[60:61], v[60:61], v[62:63]
	s_mov_b64 s[0:1], 0x410000
	v_mov_b32_dpp v76, v81 row_shr:1 row_mask:0xf bank_mask:0xf
	v_mov_b32_e32 v41, v81
	v_lshl_add_u64 v[136:137], v[134:135], 0, s[0:1]
	s_nop 1
	s_mov_b64 vcc, s[28:29]
	s_nop 0
	v_cndmask_b32_dpp v130, v60, v128, vcc quad_perm:[1,0,3,2] row_mask:0xf bank_mask:0xf
	v_cndmask_b32_dpp v131, v61, v129, vcc quad_perm:[1,0,3,2] row_mask:0xf bank_mask:0xf
	s_mov_b64 vcc, s[30:31]
	s_nop 0
	v_cndmask_b32_dpp v132, v128, v60, vcc quad_perm:[1,0,3,2] row_mask:0xf bank_mask:0xf
	v_cndmask_b32_dpp v133, v129, v61, vcc quad_perm:[1,0,3,2] row_mask:0xf bank_mask:0xf
	global_store_dwordx4 v[136:137], v[130:133], off sc0 sc1 nt
	s_nop 1
	v_pk_mul_f32 v[60:61], v[40:41], v[76:77]
	v_accvgpr_write_b32 a36, v66
	v_pk_fma_f32 v[60:61], v[80:81], v[66:67], v[60:61] op_sel_hi:[0,1,1]
	v_accvgpr_write_b32 a37, v67
	v_accvgpr_read_b32 v67, a29
	v_accvgpr_write_b32 a5, v2
	v_accvgpr_write_b32 a38, v100
	v_accvgpr_read_b32 v66, a28
	v_mov_b32_e32 v2, v35
	v_accvgpr_write_b32 a39, v101
	v_mov_b32_dpp v11, v80 row_shl:1 row_mask:0xf bank_mask:0xf
	v_pk_mov_b32 v[62:63], v[80:81], v[66:67] op_sel:[1,0]
	v_mov_b32_dpp v2, v85 row_shr:1 row_mask:0xf bank_mask:0xf
	v_mov_b32_e32 v23, v85
	v_accvgpr_read_b32 v101, a33
	v_pk_fma_f32 v[60:61], v[62:63], v[10:11], v[60:61]
	v_pk_mul_f32 v[62:63], v[22:23], v[2:3]
	v_accvgpr_read_b32 v100, a32
	v_mov_b32_dpp v35, v84 row_shl:1 row_mask:0xf bank_mask:0xf
	v_pk_fma_f32 v[62:63], v[84:85], v[100:101], v[62:63] op_sel_hi:[0,1,1]
	v_pk_mov_b32 v[68:69], v[84:85], v[8:9] op_sel:[1,0]
	v_mov_b32_e32 v92, v59
	v_pk_fma_f32 v[62:63], v[68:69], v[34:35], v[62:63]
	v_pk_add_f32 v[60:61], v[60:61], 0 op_sel_hi:[1,0]
	v_mov_b32_dpp v92, v127 row_shr:1 row_mask:0xf bank_mask:0xf
	v_mov_b32_e32 v97, v127
	v_accvgpr_read_b32 v17, a9
	v_accvgpr_read_b32 v71, a49
	v_pk_add_f32 v[60:61], v[60:61], v[62:63]
	v_pk_mul_f32 v[62:63], v[96:97], v[92:93]
	v_accvgpr_read_b32 v16, a8
	v_accvgpr_read_b32 v70, a48
	v_mov_b32_dpp v59, v126 row_shl:1 row_mask:0xf bank_mask:0xf
	v_pk_fma_f32 v[62:63], v[126:127], v[16:17], v[62:63] op_sel_hi:[0,1,1]
	v_pk_mov_b32 v[68:69], v[126:127], v[70:71] op_sel:[1,0]
	v_mov_b32_e32 v94, v57
	v_pk_fma_f32 v[62:63], v[68:69], v[58:59], v[62:63]
	v_accvgpr_write_b32 a20, v28
	v_pk_add_f32 v[60:61], v[60:61], v[62:63]
	s_mov_b64 s[0:1], 0x420000
	v_mov_b32_dpp v94, v125 row_shr:1 row_mask:0xf bank_mask:0xf
	v_mov_b32_e32 v99, v125
	v_accvgpr_read_b32 v29, a3
	v_lshl_add_u64 v[62:63], v[54:55], 0, s[0:1]
	v_mov_b32_e32 v128, v60
	v_mov_b32_e32 v129, v61
	v_pk_mul_f32 v[60:61], v[98:99], v[94:95]
	v_accvgpr_read_b32 v28, a2
	v_mov_b32_e32 v102, v51
	v_mov_b32_dpp v57, v124 row_shl:1 row_mask:0xf bank_mask:0xf
	v_pk_fma_f32 v[60:61], v[124:125], v[28:29], v[60:61] op_sel_hi:[0,1,1]
	v_mov_b32_e32 v62, v125
	v_mov_b32_e32 v63, v67
	v_mov_b32_dpp v102, v123 row_shr:1 row_mask:0xf bank_mask:0xf
	v_mov_b32_e32 v105, v123
	v_pk_fma_f32 v[60:61], v[62:63], v[56:57], v[60:61]
	v_pk_mul_f32 v[62:63], v[104:105], v[102:103]
	v_mov_b32_dpp v51, v122 row_shl:1 row_mask:0xf bank_mask:0xf
	v_pk_fma_f32 v[62:63], v[122:123], v[30:31], v[62:63] op_sel_hi:[0,1,1]
	v_accvgpr_write_b32 a28, v30
	v_mov_b32_e32 v68, v123
	v_mov_b32_e32 v69, v9
	v_mov_b32_e32 v108, v49
	v_accvgpr_write_b32 a29, v31
	v_pk_fma_f32 v[62:63], v[68:69], v[50:51], v[62:63]
	v_pk_add_f32 v[60:61], v[60:61], 0 op_sel_hi:[1,0]
	v_mov_b32_dpp v108, v121 row_shr:1 row_mask:0xf bank_mask:0xf
	v_mov_b32_e32 v111, v121
	v_accvgpr_read_b32 v31, a7
	v_pk_add_f32 v[60:61], v[60:61], v[62:63]
	v_pk_mul_f32 v[62:63], v[110:111], v[108:109]
	v_accvgpr_read_b32 v30, a6
	v_mov_b32_dpp v49, v120 row_shl:1 row_mask:0xf bank_mask:0xf
	v_pk_fma_f32 v[62:63], v[120:121], v[30:31], v[62:63] op_sel_hi:[0,1,1]
	v_mov_b32_e32 v68, v121
	v_mov_b32_e32 v69, v71
	v_pk_fma_f32 v[62:63], v[68:69], v[48:49], v[62:63]
	s_mov_b64 s[0:1], 0x430000
	v_pk_add_f32 v[60:61], v[60:61], v[62:63]
	v_lshl_add_u64 v[136:137], v[134:135], 0, s[0:1]
	v_add_u32_e32 v1, s16, v118
	s_add_u32 s0, s10, 0x1800000
	v_accvgpr_write_b32 a26, v114
	s_nop 1
	s_mov_b64 vcc, s[28:29]
	s_nop 0
	v_cndmask_b32_dpp v130, v60, v128, vcc quad_perm:[1,0,3,2] row_mask:0xf bank_mask:0xf
	v_cndmask_b32_dpp v131, v61, v129, vcc quad_perm:[1,0,3,2] row_mask:0xf bank_mask:0xf
	s_mov_b64 vcc, s[30:31]
	s_nop 0
	v_cndmask_b32_dpp v132, v128, v60, vcc quad_perm:[1,0,3,2] row_mask:0xf bank_mask:0xf
	v_cndmask_b32_dpp v133, v129, v61, vcc quad_perm:[1,0,3,2] row_mask:0xf bank_mask:0xf
	global_store_dwordx4 v[136:137], v[130:133], off sc0 sc1 nt
	s_nop 1
	v_readfirstlane_b32 s2, v1
	s_addc_u32 s1, s11, 0
	v_add_u32_e32 v1, s16, v90
	v_accvgpr_write_b32 a18, v116
	v_accvgpr_write_b32 a27, v115
	s_waitcnt vmcnt(16)
	v_lshl_add_u64 v[60:61], s[0:1], 0, v[32:33]
	s_mov_b32 m0, s2
	v_readfirstlane_b32 s2, v1
	v_add_u32_e32 v1, s16, v91
	v_accvgpr_read_b32 v115, a23
	v_accvgpr_write_b32 a19, v117
	s_waitcnt lgkmcnt(0)
	s_barrier
	global_load_lds_dwordx4 v[60:61], off nt
	v_lshl_add_u64 v[60:61], s[0:1], 0, v[74:75]
	s_mov_b32 m0, s2
	v_readfirstlane_b32 s2, v1
	v_accvgpr_read_b32 v114, a22
	v_add_u32_e32 v1, s16, v119
	v_accvgpr_read_b32 v117, a31
	global_load_lds_dwordx4 v[60:61], off nt
	v_lshl_add_u64 v[60:61], s[0:1], 0, v[114:115]
	s_mov_b32 m0, s2
	v_readfirstlane_b32 s2, v1
	v_accvgpr_read_b32 v116, a30
	global_load_lds_dwordx4 v[60:61], off nt
	v_lshl_add_u64 v[60:61], s[0:1], 0, v[116:117]
	s_mov_b32 m0, s2
	v_accvgpr_write_b32 a1, v5
	global_load_lds_dwordx4 v[60:61], off nt
	v_accvgpr_read_b32 v5, a10
	v_add_u32_e32 v2, 16, v5
	ds_read_b64 v[60:61], v2
	ds_read_b64 v[62:63], v2 offset:288
	ds_read_b64 v[68:69], v2 offset:576
	ds_read_b64 v[70:71], v2 offset:1728
	ds_read_b64 v[72:73], v2 offset:2016
	ds_read_b64 v[82:83], v2 offset:2304
	ds_read_b64 v[80:81], v2 offset:3456
	ds_read_b64 v[84:85], v2 offset:3744
	ds_read_b64 v[124:125], v2 offset:4032
	ds_read_b64 v[122:123], v2 offset:5184
	ds_read_b64 v[120:121], v2 offset:5472
	ds_read_b64 v[90:91], v2 offset:5760
	ds_read_b32 v43, v4
	ds_read_b32 v19, v4 offset:288
	ds_read_b32 v39, v4 offset:576
	ds_read_b32 v25, v4 offset:1728
	ds_read_b32 v7, v4 offset:2016
	ds_read_b32 v21, v4 offset:2304
	ds_read_b32 v11, v4 offset:3456
	ds_read_b32 v35, v4 offset:3744
	ds_read_b32 v59, v4 offset:4032
	ds_read_b32 v57, v4 offset:5184
	ds_read_b32 v51, v4 offset:5472
	ds_read_b32 v49, v4 offset:5760
	s_waitcnt lgkmcnt(0)
	v_accvgpr_write_b32 a46, v88
	v_mov_b32_e32 v46, v43
	v_accvgpr_write_b32 a8, v8
	v_mov_b32_e32 v113, v61
	v_mov_b32_dpp v46, v61 row_shr:1 row_mask:0xf bank_mask:0xf
	v_accvgpr_mov_b32 a42, a52
	v_accvgpr_write_b32 a47, v89
	v_accvgpr_write_b32 a9, v9
	v_pk_mul_f32 v[88:89], v[112:113], v[46:47]
	v_accvgpr_write_b32 a40, v112
	v_accvgpr_read_b32 v8, a18
	v_accvgpr_read_b32 v113, a39
	v_accvgpr_mov_b32 a43, a53
	v_accvgpr_write_b32 a51, v33
	v_accvgpr_write_b32 a52, v74
	v_accvgpr_read_b32 v9, a19
	v_accvgpr_read_b32 v112, a38
	v_mov_b32_e32 v26, v19
	v_accvgpr_write_b32 a50, v32
	v_accvgpr_write_b32 a53, v75
	v_mov_b32_dpp v43, v60 row_shl:1 row_mask:0xf bank_mask:0xf
	v_pk_fma_f32 v[88:89], v[60:61], v[8:9], v[88:89] op_sel_hi:[0,1,1]
	v_pk_mov_b32 v[60:61], v[60:61], v[112:113] op_sel:[1,0]
	v_mov_b32_dpp v26, v63 row_shr:1 row_mask:0xf bank_mask:0xf
	v_accvgpr_read_b32 v32, a34
	v_mov_b32_e32 v33, v63
	v_accvgpr_read_b32 v127, a27
	v_accvgpr_read_b32 v75, a43
	v_pk_fma_f32 v[60:61], v[60:61], v[42:43], v[88:89]
	v_pk_mul_f32 v[88:89], v[32:33], v[26:27]
	v_accvgpr_read_b32 v126, a26
	v_accvgpr_read_b32 v74, a42
	v_mov_b32_dpp v19, v62 row_shl:1 row_mask:0xf bank_mask:0xf
	v_pk_fma_f32 v[88:89], v[62:63], v[126:127], v[88:89] op_sel_hi:[0,1,1]
	v_pk_mov_b32 v[62:63], v[62:63], v[74:75] op_sel:[1,0]
	v_mov_b32_e32 v44, v39
	v_accvgpr_mov_b32 a14, a48
	v_pk_fma_f32 v[62:63], v[62:63], v[18:19], v[88:89]
	v_pk_add_f32 v[60:61], v[60:61], 0 op_sel_hi:[1,0]
	v_mov_b32_dpp v44, v69 row_shr:1 row_mask:0xf bank_mask:0xf
	v_mov_b32_e32 v1, v69
	v_accvgpr_mov_b32 a15, a49
	v_pk_add_f32 v[60:61], v[60:61], v[62:63]
	v_pk_mul_f32 v[62:63], v[0:1], v[44:45]
	v_accvgpr_write_b32 a48, v0
	v_accvgpr_read_b32 v89, a45
	v_accvgpr_read_b32 v0, a46
	v_accvgpr_read_b32 v88, a44
	v_accvgpr_read_b32 v1, a47
	v_mov_b32_dpp v39, v68 row_shl:1 row_mask:0xf bank_mask:0xf
	v_pk_fma_f32 v[62:63], v[68:69], v[88:89], v[62:63] op_sel_hi:[0,1,1]
	v_pk_mov_b32 v[68:69], v[68:69], v[0:1] op_sel:[1,0]
	v_mov_b32_e32 v36, v25
	v_pk_fma_f32 v[62:63], v[68:69], v[38:39], v[62:63]
	s_mov_b64 s[0:1], 0x800000
	v_pk_add_f32 v[60:61], v[60:61], v[62:63]
	v_mov_b32_dpp v36, v71 row_shr:1 row_mask:0xf bank_mask:0xf
	v_mov_b32_e32 v65, v71
	v_lshl_add_u64 v[62:63], v[54:55], 0, s[0:1]
	v_mov_b32_e32 v128, v60
	v_mov_b32_e32 v129, v61
	v_pk_mul_f32 v[60:61], v[64:65], v[36:37]
	v_mov_b64_e32 v[118:119], v[86:87]
	v_mov_b32_e32 v12, v7
	v_accvgpr_write_b32 a24, v32
	v_mov_b32_dpp v25, v70 row_shl:1 row_mask:0xf bank_mask:0xf
	v_pk_fma_f32 v[60:61], v[70:71], v[118:119], v[60:61] op_sel_hi:[0,1,1]
	v_mov_b32_e32 v62, v71
	v_mov_b32_e32 v63, v113
	v_mov_b32_dpp v12, v73 row_shr:1 row_mask:0xf bank_mask:0xf
	v_accvgpr_read_b32 v32, a20
	v_mov_b32_e32 v33, v73
	v_pk_fma_f32 v[60:61], v[62:63], v[24:25], v[60:61]
	v_pk_mul_f32 v[62:63], v[32:33], v[12:13]
	v_mov_b32_dpp v7, v72 row_shl:1 row_mask:0xf bank_mask:0xf
	v_pk_fma_f32 v[62:63], v[72:73], v[106:107], v[62:63] op_sel_hi:[0,1,1]
	v_mov_b32_e32 v68, v73
	v_mov_b32_e32 v69, v75
	v_mov_b32_e32 v78, v21
	v_pk_fma_f32 v[62:63], v[68:69], v[6:7], v[62:63]
	v_pk_add_f32 v[60:61], v[60:61], 0 op_sel_hi:[1,0]
	v_mov_b32_dpp v78, v83 row_shr:1 row_mask:0xf bank_mask:0xf
	v_mov_b32_e32 v53, v83
	v_pk_add_f32 v[60:61], v[60:61], v[62:63]
	v_pk_mul_f32 v[62:63], v[52:53], v[78:79]
	v_mov_b32_dpp v21, v82 row_shl:1 row_mask:0xf bank_mask:0xf
	v_pk_fma_f32 v[62:63], v[82:83], v[14:15], v[62:63] op_sel_hi:[0,1,1]
	v_mov_b32_e32 v68, v83
	v_mov_b32_e32 v69, v1
	v_accvgpr_write_b32 a19, v15
	v_pk_fma_f32 v[62:63], v[68:69], v[20:21], v[62:63]
	v_mov_b32_e32 v76, v11
	v_accvgpr_write_b32 a18, v14
	v_pk_add_f32 v[60:61], v[60:61], v[62:63]
	s_mov_b64 s[0:1], 0x810000
	v_mov_b32_dpp v76, v81 row_shr:1 row_mask:0xf bank_mask:0xf
	v_mov_b32_e32 v41, v81
	v_accvgpr_read_b32 v14, a36
	v_accvgpr_write_b32 a6, v2
	v_lshl_add_u64 v[136:137], v[134:135], 0, s[0:1]
	s_nop 1
	s_mov_b64 vcc, s[28:29]
	s_nop 0
	v_cndmask_b32_dpp v130, v60, v128, vcc quad_perm:[1,0,3,2] row_mask:0xf bank_mask:0xf
	v_cndmask_b32_dpp v131, v61, v129, vcc quad_perm:[1,0,3,2] row_mask:0xf bank_mask:0xf
	s_mov_b64 vcc, s[30:31]
	s_nop 0
	v_cndmask_b32_dpp v132, v128, v60, vcc quad_perm:[1,0,3,2] row_mask:0xf bank_mask:0xf
	v_cndmask_b32_dpp v133, v129, v61, vcc quad_perm:[1,0,3,2] row_mask:0xf bank_mask:0xf
	global_store_dwordx4 v[136:137], v[130:133], off sc0 sc1 nt
	s_nop 1
	v_pk_mul_f32 v[60:61], v[40:41], v[76:77]
	v_accvgpr_read_b32 v15, a37
	v_mov_b32_e32 v2, v35
	v_mov_b32_dpp v11, v80 row_shl:1 row_mask:0xf bank_mask:0xf
	v_pk_fma_f32 v[60:61], v[80:81], v[14:15], v[60:61] op_sel_hi:[0,1,1]
	v_pk_mov_b32 v[62:63], v[80:81], v[66:67] op_sel:[1,0]
	v_mov_b32_dpp v2, v85 row_shr:1 row_mask:0xf bank_mask:0xf
	v_mov_b32_e32 v23, v85
	v_accvgpr_read_b32 v15, a9
	v_pk_fma_f32 v[60:61], v[62:63], v[10:11], v[60:61]
	v_pk_mul_f32 v[62:63], v[22:23], v[2:3]
	v_accvgpr_read_b32 v14, a8
	v_mov_b32_dpp v35, v84 row_shl:1 row_mask:0xf bank_mask:0xf
	v_pk_fma_f32 v[62:63], v[84:85], v[100:101], v[62:63] op_sel_hi:[0,1,1]
	v_pk_mov_b32 v[68:69], v[84:85], v[14:15] op_sel:[1,0]
	v_mov_b32_e32 v92, v59
	v_pk_fma_f32 v[62:63], v[68:69], v[34:35], v[62:63]
	v_pk_add_f32 v[60:61], v[60:61], 0 op_sel_hi:[1,0]
	v_mov_b32_dpp v92, v125 row_shr:1 row_mask:0xf bank_mask:0xf
	v_mov_b32_e32 v97, v125
	v_accvgpr_read_b32 v71, a15
	v_pk_add_f32 v[60:61], v[60:61], v[62:63]
	v_pk_mul_f32 v[62:63], v[96:97], v[92:93]
	v_accvgpr_read_b32 v70, a14
	v_mov_b32_dpp v59, v124 row_shl:1 row_mask:0xf bank_mask:0xf
	v_pk_fma_f32 v[62:63], v[124:125], v[16:17], v[62:63] op_sel_hi:[0,1,1]
	v_pk_mov_b32 v[68:69], v[124:125], v[70:71] op_sel:[1,0]
	v_mov_b32_e32 v94, v57
	v_pk_fma_f32 v[62:63], v[68:69], v[58:59], v[62:63]
	s_mov_b64 s[0:1], 0x820000
	v_pk_add_f32 v[60:61], v[60:61], v[62:63]
	v_mov_b32_dpp v94, v123 row_shr:1 row_mask:0xf bank_mask:0xf
	v_mov_b32_e32 v99, v123
	v_accvgpr_write_b32 a31, v17
	v_lshl_add_u64 v[62:63], v[54:55], 0, s[0:1]
	v_mov_b32_e32 v128, v60
	v_mov_b32_e32 v129, v61
	v_pk_mul_f32 v[60:61], v[98:99], v[94:95]
	v_mov_b32_e32 v102, v51
	v_accvgpr_write_b32 a30, v16
	v_mov_b32_dpp v57, v122 row_shl:1 row_mask:0xf bank_mask:0xf
	v_pk_fma_f32 v[60:61], v[122:123], v[28:29], v[60:61] op_sel_hi:[0,1,1]
	v_mov_b32_e32 v62, v123
	v_mov_b32_e32 v63, v67
	v_mov_b32_dpp v102, v121 row_shr:1 row_mask:0xf bank_mask:0xf
	v_mov_b32_e32 v105, v121
	v_accvgpr_read_b32 v16, a28
	v_pk_fma_f32 v[60:61], v[62:63], v[56:57], v[60:61]
	v_pk_mul_f32 v[62:63], v[104:105], v[102:103]
	v_accvgpr_read_b32 v17, a29
	v_mov_b32_dpp v51, v120 row_shl:1 row_mask:0xf bank_mask:0xf
	v_pk_fma_f32 v[62:63], v[120:121], v[16:17], v[62:63] op_sel_hi:[0,1,1]
	v_mov_b32_e32 v68, v121
	v_mov_b32_e32 v69, v15
	v_mov_b32_e32 v108, v49
	v_pk_fma_f32 v[62:63], v[68:69], v[50:51], v[62:63]
	v_pk_add_f32 v[60:61], v[60:61], 0 op_sel_hi:[1,0]
	v_mov_b32_dpp v108, v91 row_shr:1 row_mask:0xf bank_mask:0xf
	v_mov_b32_e32 v111, v91
	v_pk_add_f32 v[60:61], v[60:61], v[62:63]
	v_pk_mul_f32 v[62:63], v[110:111], v[108:109]
	v_mov_b32_dpp v49, v90 row_shl:1 row_mask:0xf bank_mask:0xf
	v_pk_fma_f32 v[62:63], v[90:91], v[30:31], v[62:63] op_sel_hi:[0,1,1]
	v_mov_b32_e32 v68, v91
	v_mov_b32_e32 v69, v71
	v_pk_fma_f32 v[62:63], v[68:69], v[48:49], v[62:63]
	s_mov_b64 s[0:1], 0x830000
	v_mov_b32_e32 v0, v22
	v_pk_add_f32 v[60:61], v[60:61], v[62:63]
	v_lshl_add_u64 v[136:137], v[134:135], 0, s[0:1]
	s_add_u32 s0, s10, 0x1c00000
	v_accvgpr_read_b32 v22, a50
	v_accvgpr_read_b32 v1, a72
	s_addc_u32 s1, s11, 0
	v_accvgpr_read_b32 v23, a51
	s_nop 1
	s_mov_b64 vcc, s[28:29]
	s_nop 0
	v_cndmask_b32_dpp v130, v60, v128, vcc quad_perm:[1,0,3,2] row_mask:0xf bank_mask:0xf
	v_cndmask_b32_dpp v131, v61, v129, vcc quad_perm:[1,0,3,2] row_mask:0xf bank_mask:0xf
	s_mov_b64 vcc, s[30:31]
	s_nop 0
	v_cndmask_b32_dpp v132, v128, v60, vcc quad_perm:[1,0,3,2] row_mask:0xf bank_mask:0xf
	v_cndmask_b32_dpp v133, v129, v61, vcc quad_perm:[1,0,3,2] row_mask:0xf bank_mask:0xf
	global_store_dwordx4 v[136:137], v[130:133], off sc0 sc1 nt
	s_nop 1
	v_readfirstlane_b32 s2, v1
	v_lshl_add_u64 v[60:61], s[0:1], 0, v[22:23]
	v_accvgpr_read_b32 v1, a12
	v_accvgpr_read_b32 v22, a52
	s_waitcnt vmcnt(18)
	s_mov_b32 m0, s2
	v_readfirstlane_b32 s2, v1
	v_accvgpr_read_b32 v23, a53
	v_accvgpr_read_b32 v1, a13
	s_waitcnt lgkmcnt(0)
	s_barrier
	global_load_lds_dwordx4 v[60:61], off nt
	v_lshl_add_u64 v[60:61], s[0:1], 0, v[22:23]
	s_mov_b32 m0, s2
	v_readfirstlane_b32 s2, v1
	v_accvgpr_read_b32 v1, a16
	global_load_lds_dwordx4 v[60:61], off nt
	v_lshl_add_u64 v[60:61], s[0:1], 0, v[114:115]
	s_mov_b32 m0, s2
	v_readfirstlane_b32 s2, v1
	global_load_lds_dwordx4 v[60:61], off nt
	v_lshl_add_u64 v[60:61], s[0:1], 0, v[116:117]
	s_mov_b32 m0, s2
	v_accvgpr_write_b32 a22, v30
	v_accvgpr_write_b32 a44, v70
	global_load_lds_dwordx4 v[60:61], off nt
	v_accvgpr_write_b32 a2, v106
	v_accvgpr_write_b32 a34, v74
	v_accvgpr_write_b32 a23, v31
	v_accvgpr_write_b32 a45, v71
	v_add_u32_e32 v2, 0x7010, v5
	v_mov_b32_e32 v31, v5
	v_add_u32_e32 v5, 0x7000, v4
	ds_read_b64 v[60:61], v2
	ds_read_b64 v[62:63], v2 offset:288
	ds_read_b64 v[68:69], v2 offset:576
	ds_read_b64 v[70:71], v2 offset:1728
	ds_read_b64 v[72:73], v2 offset:2016
	ds_read_b64 v[82:83], v2 offset:2304
	ds_read_b64 v[80:81], v2 offset:3456
	ds_read_b64 v[84:85], v2 offset:3744
	ds_read_b64 v[116:117], v2 offset:4032
	ds_read_b64 v[114:115], v2 offset:5184
	ds_read_b64 v[112:113], v2 offset:5472
	ds_read_b64 v[90:91], v2 offset:5760
	ds_read_b32 v43, v5
	ds_read_b32 v19, v5 offset:288
	ds_read_b32 v39, v5 offset:576
	ds_read_b32 v25, v5 offset:1728
	ds_read_b32 v7, v5 offset:2016
	ds_read_b32 v21, v5 offset:2304
	ds_read_b32 v11, v5 offset:3456
	ds_read_b32 v35, v5 offset:3744
	ds_read_b32 v59, v5 offset:4032
	ds_read_b32 v57, v5 offset:5184
	ds_read_b32 v51, v5 offset:5472
	ds_read_b32 v49, v5 offset:5760
	s_waitcnt lgkmcnt(0)
	v_accvgpr_write_b32 a3, v107
	v_mov_b32_e32 v46, v43
	v_accvgpr_write_b32 a35, v75
	v_accvgpr_read_b32 v74, a40
	v_mov_b32_dpp v46, v61 row_shr:1 row_mask:0xf bank_mask:0xf
	v_mov_b32_e32 v75, v61
	v_accvgpr_read_b32 v107, a39
	v_accvgpr_write_b32 a10, v100
	v_pk_mul_f32 v[86:87], v[74:75], v[46:47]
	v_accvgpr_read_b32 v106, a38
	v_mov_b32_e32 v26, v19
	v_accvgpr_write_b32 a11, v101
	v_mov_b32_dpp v43, v60 row_shl:1 row_mask:0xf bank_mask:0xf
	v_mov_b32_e32 v32, v74
	v_pk_fma_f32 v[86:87], v[60:61], v[8:9], v[86:87] op_sel_hi:[0,1,1]
	v_pk_mov_b32 v[60:61], v[60:61], v[106:107] op_sel:[1,0]
	v_mov_b32_dpp v26, v63 row_shr:1 row_mask:0xf bank_mask:0xf
	v_accvgpr_read_b32 v74, a24
	v_mov_b32_e32 v75, v63
	v_accvgpr_read_b32 v101, a35
	v_pk_fma_f32 v[60:61], v[60:61], v[42:43], v[86:87]
	v_pk_mul_f32 v[86:87], v[74:75], v[26:27]
	v_accvgpr_read_b32 v100, a34
	v_accvgpr_write_b32 a14, v66
	v_mov_b32_dpp v19, v62 row_shl:1 row_mask:0xf bank_mask:0xf
	v_pk_fma_f32 v[86:87], v[62:63], v[126:127], v[86:87] op_sel_hi:[0,1,1]
	v_pk_mov_b32 v[62:63], v[62:63], v[100:101] op_sel:[1,0]
	v_mov_b32_e32 v44, v39
	v_accvgpr_write_b32 a42, v64
	v_accvgpr_write_b32 a15, v67
	v_mov_b32_e32 v66, v4
	v_pk_fma_f32 v[62:63], v[62:63], v[18:19], v[86:87]
	v_pk_add_f32 v[60:61], v[60:61], 0 op_sel_hi:[1,0]
	v_mov_b32_dpp v44, v69 row_shr:1 row_mask:0xf bank_mask:0xf
	v_accvgpr_read_b32 v64, a48
	v_mov_b32_e32 v65, v69
	v_accvgpr_read_b32 v4, a46
	v_pk_add_f32 v[60:61], v[60:61], v[62:63]
	v_pk_mul_f32 v[62:63], v[64:65], v[44:45]
	v_accvgpr_read_b32 v5, a47
	v_mov_b32_dpp v39, v68 row_shl:1 row_mask:0xf bank_mask:0xf
	v_pk_fma_f32 v[62:63], v[68:69], v[88:89], v[62:63] op_sel_hi:[0,1,1]
	v_pk_mov_b32 v[68:69], v[68:69], v[4:5] op_sel:[1,0]
	v_mov_b32_e32 v36, v25
	v_pk_fma_f32 v[62:63], v[68:69], v[38:39], v[62:63]
	s_mov_b64 s[0:1], 0xc00000
	v_pk_add_f32 v[60:61], v[60:61], v[62:63]
	v_mov_b32_dpp v36, v71 row_shr:1 row_mask:0xf bank_mask:0xf
	v_accvgpr_read_b32 v22, a42
	v_mov_b32_e32 v23, v71
	v_accvgpr_mov_b32 a26, a20
	v_accvgpr_write_b32 a20, v28
	v_lshl_add_u64 v[62:63], v[54:55], 0, s[0:1]
	v_mov_b32_e32 v128, v60
	v_mov_b32_e32 v129, v61
	v_pk_mul_f32 v[60:61], v[22:23], v[36:37]
	v_mov_b32_e32 v12, v7
	v_accvgpr_write_b32 a21, v29
	v_mov_b32_dpp v25, v70 row_shl:1 row_mask:0xf bank_mask:0xf
	v_pk_fma_f32 v[60:61], v[70:71], v[118:119], v[60:61] op_sel_hi:[0,1,1]
	v_mov_b32_e32 v62, v71
	v_mov_b32_e32 v63, v107
	v_mov_b32_dpp v12, v73 row_shr:1 row_mask:0xf bank_mask:0xf
	v_accvgpr_read_b32 v28, a26
	v_mov_b32_e32 v29, v73
	v_accvgpr_read_b32 v121, a3
	v_pk_fma_f32 v[60:61], v[62:63], v[24:25], v[60:61]
	v_pk_mul_f32 v[62:63], v[28:29], v[12:13]
	v_accvgpr_read_b32 v120, a2
	v_mov_b32_dpp v7, v72 row_shl:1 row_mask:0xf bank_mask:0xf
	v_pk_fma_f32 v[62:63], v[72:73], v[120:121], v[62:63] op_sel_hi:[0,1,1]
	v_mov_b32_e32 v68, v73
	v_mov_b32_e32 v69, v101
	v_mov_b32_e32 v78, v21
	v_pk_fma_f32 v[62:63], v[68:69], v[6:7], v[62:63]
	v_pk_add_f32 v[60:61], v[60:61], 0 op_sel_hi:[1,0]
	v_mov_b32_dpp v78, v83 row_shr:1 row_mask:0xf bank_mask:0xf
	v_mov_b32_e32 v53, v83
	v_accvgpr_read_b32 v125, a19
	v_pk_add_f32 v[60:61], v[60:61], v[62:63]
	v_pk_mul_f32 v[62:63], v[52:53], v[78:79]
	v_accvgpr_read_b32 v124, a18
	v_mov_b32_dpp v21, v82 row_shl:1 row_mask:0xf bank_mask:0xf
	v_pk_fma_f32 v[62:63], v[82:83], v[124:125], v[62:63] op_sel_hi:[0,1,1]
	v_mov_b32_e32 v68, v83
	v_mov_b32_e32 v69, v5
	v_pk_fma_f32 v[62:63], v[68:69], v[20:21], v[62:63]
	v_mov_b32_e32 v76, v11
	v_pk_add_f32 v[60:61], v[60:61], v[62:63]
	s_mov_b64 s[0:1], 0xc10000
	v_mov_b32_dpp v76, v81 row_shr:1 row_mask:0xf bank_mask:0xf
	v_mov_b32_e32 v41, v81
	v_accvgpr_read_b32 v123, a37
	v_accvgpr_read_b32 v4, a14
	v_lshl_add_u64 v[136:137], v[134:135], 0, s[0:1]
	s_nop 1
	s_mov_b64 vcc, s[28:29]
	s_nop 0
	v_cndmask_b32_dpp v130, v60, v128, vcc quad_perm:[1,0,3,2] row_mask:0xf bank_mask:0xf
	v_cndmask_b32_dpp v131, v61, v129, vcc quad_perm:[1,0,3,2] row_mask:0xf bank_mask:0xf
	s_mov_b64 vcc, s[30:31]
	s_nop 0
	v_cndmask_b32_dpp v132, v128, v60, vcc quad_perm:[1,0,3,2] row_mask:0xf bank_mask:0xf
	v_cndmask_b32_dpp v133, v129, v61, vcc quad_perm:[1,0,3,2] row_mask:0xf bank_mask:0xf
	global_store_dwordx4 v[136:137], v[130:133], off sc0 sc1 nt
	s_nop 1
	v_pk_mul_f32 v[60:61], v[40:41], v[76:77]
	v_accvgpr_read_b32 v122, a36
	v_accvgpr_read_b32 v5, a15
	v_mov_b32_e32 v2, v35
	v_accvgpr_mov_b32 a32, a24
	v_accvgpr_write_b32 a24, v22
	v_mov_b64_e32 v[22:23], v[118:119]
	v_mov_b32_dpp v11, v80 row_shl:1 row_mask:0xf bank_mask:0xf
	v_pk_fma_f32 v[60:61], v[80:81], v[122:123], v[60:61] op_sel_hi:[0,1,1]
	v_pk_mov_b32 v[62:63], v[80:81], v[4:5] op_sel:[1,0]
	v_mov_b32_dpp v2, v85 row_shr:1 row_mask:0xf bank_mask:0xf
	v_mov_b32_e32 v106, v0
	v_mov_b32_e32 v107, v85
	v_accvgpr_read_b32 v119, a11
	v_pk_fma_f32 v[60:61], v[62:63], v[10:11], v[60:61]
	v_pk_mul_f32 v[62:63], v[106:107], v[2:3]
	v_accvgpr_read_b32 v118, a10
	v_mov_b64_e32 v[100:101], v[14:15]
	v_mov_b32_dpp v35, v84 row_shl:1 row_mask:0xf bank_mask:0xf
	v_pk_fma_f32 v[62:63], v[84:85], v[118:119], v[62:63] op_sel_hi:[0,1,1]
	v_pk_mov_b32 v[68:69], v[84:85], v[100:101] op_sel:[1,0]
	v_mov_b32_e32 v92, v59
	v_accvgpr_write_b32 a26, v52
	v_mov_b32_e32 v74, v40
	v_pk_fma_f32 v[62:63], v[68:69], v[34:35], v[62:63]
	v_pk_add_f32 v[60:61], v[60:61], 0 op_sel_hi:[1,0]
	v_mov_b32_dpp v92, v117 row_shr:1 row_mask:0xf bank_mask:0xf
	v_mov_b32_e32 v97, v117
	v_accvgpr_read_b32 v41, a31
	v_accvgpr_read_b32 v53, a45
	v_pk_add_f32 v[60:61], v[60:61], v[62:63]
	v_pk_mul_f32 v[62:63], v[96:97], v[92:93]
	v_accvgpr_read_b32 v40, a30
	v_accvgpr_read_b32 v52, a44
	v_mov_b32_dpp v59, v116 row_shl:1 row_mask:0xf bank_mask:0xf
	v_pk_fma_f32 v[62:63], v[116:117], v[40:41], v[62:63] op_sel_hi:[0,1,1]
	v_pk_mov_b32 v[68:69], v[116:117], v[52:53] op_sel:[1,0]
	v_mov_b32_e32 v94, v57
	v_pk_fma_f32 v[62:63], v[68:69], v[58:59], v[62:63]
	s_mov_b64 s[0:1], 0xc20000
	v_pk_add_f32 v[60:61], v[60:61], v[62:63]
	v_mov_b32_dpp v94, v115 row_shr:1 row_mask:0xf bank_mask:0xf
	v_mov_b32_e32 v99, v115
	v_accvgpr_read_b32 v14, a20
	v_lshl_add_u64 v[62:63], v[54:55], 0, s[0:1]
	v_mov_b32_e32 v128, v60
	v_mov_b32_e32 v129, v61
	v_pk_mul_f32 v[60:61], v[98:99], v[94:95]
	v_accvgpr_read_b32 v15, a21
	v_mov_b32_e32 v102, v51
	v_mov_b32_dpp v57, v114 row_shl:1 row_mask:0xf bank_mask:0xf
	v_pk_fma_f32 v[60:61], v[114:115], v[14:15], v[60:61] op_sel_hi:[0,1,1]
	v_mov_b32_e32 v62, v115
	v_mov_b32_e32 v63, v5
	v_mov_b32_dpp v102, v113 row_shr:1 row_mask:0xf bank_mask:0xf
	v_mov_b32_e32 v105, v113
	v_pk_fma_f32 v[60:61], v[62:63], v[56:57], v[60:61]
	v_pk_mul_f32 v[62:63], v[104:105], v[102:103]
	v_accvgpr_write_b32 a8, v8
	v_mov_b32_dpp v51, v112 row_shl:1 row_mask:0xf bank_mask:0xf
	v_pk_fma_f32 v[62:63], v[112:113], v[16:17], v[62:63] op_sel_hi:[0,1,1]
	v_mov_b32_e32 v68, v113
	v_mov_b32_e32 v69, v101
	v_mov_b32_e32 v108, v49
	v_accvgpr_write_b32 a9, v9
	v_pk_fma_f32 v[62:63], v[68:69], v[50:51], v[62:63]
	v_pk_add_f32 v[60:61], v[60:61], 0 op_sel_hi:[1,0]
	v_mov_b32_dpp v108, v91 row_shr:1 row_mask:0xf bank_mask:0xf
	v_mov_b32_e32 v111, v91
	v_accvgpr_read_b32 v8, a22
	v_pk_add_f32 v[60:61], v[60:61], v[62:63]
	v_pk_mul_f32 v[62:63], v[110:111], v[108:109]
	v_accvgpr_read_b32 v9, a23
	v_mov_b32_dpp v49, v90 row_shl:1 row_mask:0xf bank_mask:0xf
	v_pk_fma_f32 v[62:63], v[90:91], v[8:9], v[62:63] op_sel_hi:[0,1,1]
	v_mov_b32_e32 v68, v91
	v_mov_b32_e32 v69, v53
	v_pk_fma_f32 v[62:63], v[68:69], v[48:49], v[62:63]
	s_mov_b64 s[0:1], 0xc30000
	v_pk_add_f32 v[60:61], v[60:61], v[62:63]
	v_lshl_add_u64 v[136:137], v[134:135], 0, s[0:1]
	s_nop 1
	s_mov_b64 vcc, s[28:29]
	s_nop 0
	v_cndmask_b32_dpp v130, v60, v128, vcc quad_perm:[1,0,3,2] row_mask:0xf bank_mask:0xf
	v_cndmask_b32_dpp v131, v61, v129, vcc quad_perm:[1,0,3,2] row_mask:0xf bank_mask:0xf
	s_mov_b64 vcc, s[30:31]
	s_nop 0
	v_cndmask_b32_dpp v132, v128, v60, vcc quad_perm:[1,0,3,2] row_mask:0xf bank_mask:0xf
	v_cndmask_b32_dpp v133, v129, v61, vcc quad_perm:[1,0,3,2] row_mask:0xf bank_mask:0xf
	global_store_dwordx4 v[136:137], v[130:133], off sc0 sc1 nt
	s_nop 1
	s_waitcnt vmcnt(20)
	v_accvgpr_write_b32 a16, v88
	v_accvgpr_write_b32 a10, v100
	s_waitcnt lgkmcnt(0)
	s_barrier
	v_add_u32_e32 v2, 0xe010, v31
	v_add_u32_e32 v5, 0xe000, v66
	ds_read_b64 v[60:61], v2
	ds_read_b64 v[62:63], v2 offset:288
	ds_read_b64 v[68:69], v2 offset:576
	ds_read_b64 v[70:71], v2 offset:1728
	ds_read_b64 v[72:73], v2 offset:2016
	ds_read_b64 v[82:83], v2 offset:2304
	ds_read_b64 v[80:81], v2 offset:3456
	ds_read_b64 v[84:85], v2 offset:3744
	ds_read_b64 v[116:117], v2 offset:4032
	ds_read_b64 v[114:115], v2 offset:5184
	ds_read_b64 v[112:113], v2 offset:5472
	ds_read_b64 v[90:91], v2 offset:5760
	ds_read_b32 v43, v5
	ds_read_b32 v19, v5 offset:288
	ds_read_b32 v39, v5 offset:576
	ds_read_b32 v25, v5 offset:1728
	ds_read_b32 v7, v5 offset:2016
	ds_read_b32 v21, v5 offset:2304
	ds_read_b32 v11, v5 offset:3456
	ds_read_b32 v35, v5 offset:3744
	ds_read_b32 v59, v5 offset:4032
	ds_read_b32 v57, v5 offset:5184
	ds_read_b32 v51, v5 offset:5472
	ds_read_b32 v49, v5 offset:5760
	s_waitcnt lgkmcnt(0)
	v_accvgpr_write_b32 a17, v89
	v_mov_b32_e32 v46, v43
	v_accvgpr_write_b32 a11, v101
	v_mov_b32_e32 v33, v61
	v_mov_b32_dpp v46, v61 row_shr:1 row_mask:0xf bank_mask:0xf
	v_accvgpr_read_b32 v89, a9
	v_accvgpr_read_b32 v101, a39
	v_pk_mul_f32 v[86:87], v[32:33], v[46:47]
	v_accvgpr_read_b32 v88, a8
	v_accvgpr_read_b32 v100, a38
	v_mov_b32_e32 v26, v19
	v_accvgpr_write_b32 a19, v17
	v_mov_b32_dpp v43, v60 row_shl:1 row_mask:0xf bank_mask:0xf
	v_pk_fma_f32 v[86:87], v[60:61], v[88:89], v[86:87] op_sel_hi:[0,1,1]
	v_pk_mov_b32 v[60:61], v[60:61], v[100:101] op_sel:[1,0]
	v_mov_b32_dpp v26, v63 row_shr:1 row_mask:0xf bank_mask:0xf
	v_accvgpr_read_b32 v0, a32
	v_mov_b32_e32 v1, v63
	v_accvgpr_read_b32 v4, a34
	v_accvgpr_write_b32 a18, v16
	v_pk_fma_f32 v[60:61], v[60:61], v[42:43], v[86:87]
	v_pk_mul_f32 v[86:87], v[0:1], v[26:27]
	v_mov_b64_e32 v[16:17], v[126:127]
	v_accvgpr_read_b32 v5, a35
	v_mov_b32_dpp v19, v62 row_shl:1 row_mask:0xf bank_mask:0xf
	v_pk_fma_f32 v[86:87], v[62:63], v[16:17], v[86:87] op_sel_hi:[0,1,1]
	v_pk_mov_b32 v[62:63], v[62:63], v[4:5] op_sel:[1,0]
	v_mov_b32_e32 v44, v39
	v_accvgpr_read_b32 v30, a48
	v_mov_b32_e32 v64, v28
	v_accvgpr_write_b32 a7, v66
	v_pk_fma_f32 v[62:63], v[62:63], v[18:19], v[86:87]
	v_pk_add_f32 v[60:61], v[60:61], 0 op_sel_hi:[1,0]
	v_mov_b32_dpp v44, v69 row_shr:1 row_mask:0xf bank_mask:0xf
	v_mov_b32_e32 v31, v69
	v_accvgpr_read_b32 v29, a17
	v_accvgpr_read_b32 v67, a47
	v_pk_add_f32 v[60:61], v[60:61], v[62:63]
	v_pk_mul_f32 v[62:63], v[30:31], v[44:45]
	v_accvgpr_read_b32 v28, a16
	v_accvgpr_read_b32 v66, a46
	v_mov_b32_dpp v39, v68 row_shl:1 row_mask:0xf bank_mask:0xf
	v_pk_fma_f32 v[62:63], v[68:69], v[28:29], v[62:63] op_sel_hi:[0,1,1]
	v_pk_mov_b32 v[68:69], v[68:69], v[66:67] op_sel:[1,0]
	v_mov_b32_e32 v36, v25
	v_pk_fma_f32 v[62:63], v[68:69], v[38:39], v[62:63]
	s_mov_b64 s[0:1], 0x1000000
	v_pk_add_f32 v[60:61], v[60:61], v[62:63]
	v_mov_b32_dpp v36, v71 row_shr:1 row_mask:0xf bank_mask:0xf
	v_accvgpr_read_b32 v126, a24
	v_mov_b32_e32 v127, v71
	v_lshl_add_u64 v[62:63], v[54:55], 0, s[0:1]
	v_mov_b32_e32 v128, v60
	v_mov_b32_e32 v129, v61
	v_pk_mul_f32 v[60:61], v[126:127], v[36:37]
	v_mov_b32_e32 v12, v7
	v_mov_b32_dpp v25, v70 row_shl:1 row_mask:0xf bank_mask:0xf
	v_pk_fma_f32 v[60:61], v[70:71], v[22:23], v[60:61] op_sel_hi:[0,1,1]
	v_mov_b32_e32 v62, v71
	v_mov_b32_e32 v63, v101
	v_mov_b32_dpp v12, v73 row_shr:1 row_mask:0xf bank_mask:0xf
	v_mov_b32_e32 v52, v64
	v_mov_b32_e32 v53, v73
	v_pk_fma_f32 v[60:61], v[62:63], v[24:25], v[60:61]
	v_pk_mul_f32 v[62:63], v[52:53], v[12:13]
	v_mov_b32_dpp v7, v72 row_shl:1 row_mask:0xf bank_mask:0xf
	v_pk_fma_f32 v[62:63], v[72:73], v[120:121], v[62:63] op_sel_hi:[0,1,1]
	v_mov_b32_e32 v68, v73
	v_mov_b32_e32 v69, v5
	v_mov_b32_e32 v78, v21
	v_pk_fma_f32 v[62:63], v[68:69], v[6:7], v[62:63]
	v_pk_add_f32 v[60:61], v[60:61], 0 op_sel_hi:[1,0]
	v_mov_b32_dpp v78, v83 row_shr:1 row_mask:0xf bank_mask:0xf
	v_accvgpr_read_b32 v4, a26
	v_mov_b32_e32 v5, v83
	v_pk_add_f32 v[60:61], v[60:61], v[62:63]
	v_pk_mul_f32 v[62:63], v[4:5], v[78:79]
	v_mov_b32_dpp v21, v82 row_shl:1 row_mask:0xf bank_mask:0xf
	v_pk_fma_f32 v[62:63], v[82:83], v[124:125], v[62:63] op_sel_hi:[0,1,1]
	v_mov_b32_e32 v68, v83
	v_mov_b32_e32 v69, v67
	v_accvgpr_write_b32 a8, v120
	v_pk_fma_f32 v[62:63], v[68:69], v[20:21], v[62:63]
	v_mov_b32_e32 v76, v11
	v_accvgpr_write_b32 a9, v121
	v_pk_add_f32 v[60:61], v[60:61], v[62:63]
	s_mov_b64 s[0:1], 0x1010000
	v_mov_b32_dpp v76, v81 row_shr:1 row_mask:0xf bank_mask:0xf
	v_mov_b32_e32 v120, v74
	v_mov_b32_e32 v121, v81
	v_accvgpr_read_b32 v101, a15
	v_accvgpr_mov_b32 a12, a38
	v_lshl_add_u64 v[136:137], v[134:135], 0, s[0:1]
	s_nop 1
	s_mov_b64 vcc, s[28:29]
	s_nop 0
	v_cndmask_b32_dpp v130, v60, v128, vcc quad_perm:[1,0,3,2] row_mask:0xf bank_mask:0xf
	v_cndmask_b32_dpp v131, v61, v129, vcc quad_perm:[1,0,3,2] row_mask:0xf bank_mask:0xf
	s_mov_b64 vcc, s[30:31]
	s_nop 0
	v_cndmask_b32_dpp v132, v128, v60, vcc quad_perm:[1,0,3,2] row_mask:0xf bank_mask:0xf
	v_cndmask_b32_dpp v133, v129, v61, vcc quad_perm:[1,0,3,2] row_mask:0xf bank_mask:0xf
	global_store_dwordx4 v[136:137], v[130:133], off sc0 sc1 nt
	s_nop 1
	v_pk_mul_f32 v[60:61], v[120:121], v[76:77]
	v_accvgpr_read_b32 v100, a14
	v_mov_b32_e32 v2, v35
	v_accvgpr_mov_b32 a13, a39
	v_accvgpr_write_b32 a20, v22
	v_mov_b32_dpp v11, v80 row_shl:1 row_mask:0xf bank_mask:0xf
	v_pk_fma_f32 v[60:61], v[80:81], v[122:123], v[60:61] op_sel_hi:[0,1,1]
	v_pk_mov_b32 v[62:63], v[80:81], v[100:101] op_sel:[1,0]
	v_mov_b32_dpp v2, v85 row_shr:1 row_mask:0xf bank_mask:0xf
	v_mov_b32_e32 v107, v85
	v_accvgpr_read_b32 v123, a11
	v_accvgpr_write_b32 a21, v23
	v_accvgpr_read_b32 v23, a13
	v_pk_fma_f32 v[60:61], v[62:63], v[10:11], v[60:61]
	v_pk_mul_f32 v[62:63], v[106:107], v[2:3]
	v_accvgpr_read_b32 v122, a10
	v_accvgpr_read_b32 v22, a12
	v_mov_b32_dpp v35, v84 row_shl:1 row_mask:0xf bank_mask:0xf
	v_pk_fma_f32 v[62:63], v[84:85], v[118:119], v[62:63] op_sel_hi:[0,1,1]
	v_accvgpr_write_b32 a12, v118
	v_pk_mov_b32 v[68:69], v[84:85], v[122:123] op_sel:[1,0]
	v_mov_b32_e32 v92, v59
	v_accvgpr_write_b32 a13, v119
	v_pk_fma_f32 v[62:63], v[68:69], v[34:35], v[62:63]
	v_pk_add_f32 v[60:61], v[60:61], 0 op_sel_hi:[1,0]
	v_mov_b32_dpp v92, v117 row_shr:1 row_mask:0xf bank_mask:0xf
	v_mov_b32_e32 v97, v117
	v_mov_b64_e32 v[118:119], v[40:41]
	v_accvgpr_read_b32 v40, a44
	v_pk_add_f32 v[60:61], v[60:61], v[62:63]
	v_pk_mul_f32 v[62:63], v[96:97], v[92:93]
	v_accvgpr_read_b32 v41, a45
	v_mov_b32_dpp v59, v116 row_shl:1 row_mask:0xf bank_mask:0xf
	v_pk_fma_f32 v[62:63], v[116:117], v[118:119], v[62:63] op_sel_hi:[0,1,1]
	v_pk_mov_b32 v[68:69], v[116:117], v[40:41] op_sel:[1,0]
	v_mov_b32_e32 v94, v57
	v_pk_fma_f32 v[62:63], v[68:69], v[58:59], v[62:63]
	s_mov_b64 s[0:1], 0x1020000
	v_pk_add_f32 v[60:61], v[60:61], v[62:63]
	v_mov_b32_dpp v94, v115 row_shr:1 row_mask:0xf bank_mask:0xf
	v_mov_b32_e32 v99, v115
	v_lshl_add_u64 v[62:63], v[54:55], 0, s[0:1]
	v_mov_b32_e32 v128, v60
	v_mov_b32_e32 v129, v61
	v_pk_mul_f32 v[60:61], v[98:99], v[94:95]
	v_mov_b32_e32 v102, v51
	v_accvgpr_write_b32 a30, v4
	v_mov_b32_dpp v57, v114 row_shl:1 row_mask:0xf bank_mask:0xf
	v_pk_fma_f32 v[60:61], v[114:115], v[14:15], v[60:61] op_sel_hi:[0,1,1]
	v_mov_b32_e32 v62, v115
	v_mov_b32_e32 v63, v101
	v_mov_b32_dpp v102, v113 row_shr:1 row_mask:0xf bank_mask:0xf
	v_mov_b32_e32 v105, v113
	v_accvgpr_read_b32 v4, a18
	v_pk_fma_f32 v[60:61], v[62:63], v[56:57], v[60:61]
	v_pk_mul_f32 v[62:63], v[104:105], v[102:103]
	v_accvgpr_read_b32 v5, a19
	v_mov_b32_dpp v51, v112 row_shl:1 row_mask:0xf bank_mask:0xf
	v_pk_fma_f32 v[62:63], v[112:113], v[4:5], v[62:63] op_sel_hi:[0,1,1]
	v_mov_b32_e32 v68, v113
	v_mov_b32_e32 v69, v123
	v_mov_b32_e32 v108, v49
	v_pk_fma_f32 v[62:63], v[68:69], v[50:51], v[62:63]
	v_pk_add_f32 v[60:61], v[60:61], 0 op_sel_hi:[1,0]
	v_mov_b32_dpp v108, v91 row_shr:1 row_mask:0xf bank_mask:0xf
	v_mov_b32_e32 v111, v91
	v_pk_add_f32 v[60:61], v[60:61], v[62:63]
	v_pk_mul_f32 v[62:63], v[110:111], v[108:109]
	v_mov_b32_dpp v49, v90 row_shl:1 row_mask:0xf bank_mask:0xf
	v_pk_fma_f32 v[62:63], v[90:91], v[8:9], v[62:63] op_sel_hi:[0,1,1]
	v_mov_b32_e32 v68, v91
	v_mov_b32_e32 v69, v41
	v_pk_fma_f32 v[62:63], v[68:69], v[48:49], v[62:63]
	s_mov_b64 s[0:1], 0x1030000
	v_pk_add_f32 v[60:61], v[60:61], v[62:63]
	v_lshl_add_u64 v[136:137], v[134:135], 0, s[0:1]
	s_nop 1
	s_mov_b64 vcc, s[28:29]
	s_nop 0
	v_cndmask_b32_dpp v130, v60, v128, vcc quad_perm:[1,0,3,2] row_mask:0xf bank_mask:0xf
	v_cndmask_b32_dpp v131, v61, v129, vcc quad_perm:[1,0,3,2] row_mask:0xf bank_mask:0xf
	s_mov_b64 vcc, s[30:31]
	s_nop 0
	v_cndmask_b32_dpp v132, v128, v60, vcc quad_perm:[1,0,3,2] row_mask:0xf bank_mask:0xf
	v_cndmask_b32_dpp v133, v129, v61, vcc quad_perm:[1,0,3,2] row_mask:0xf bank_mask:0xf
	global_store_dwordx4 v[136:137], v[130:133], off sc0 sc1 nt
	s_nop 1
	s_waitcnt vmcnt(16)
	s_waitcnt lgkmcnt(0)
	s_barrier
	v_accvgpr_read_b32 v2, a0
	v_accvgpr_read_b32 v8, a4
	ds_read_b64 v[60:61], v8
	ds_read_b64 v[62:63], v8 offset:288
	ds_read_b64 v[68:69], v8 offset:576
	ds_read_b64 v[70:71], v8 offset:1728
	ds_read_b64 v[72:73], v8 offset:2016
	ds_read_b64 v[82:83], v8 offset:2304
	ds_read_b64 v[80:81], v8 offset:3456
	ds_read_b64 v[84:85], v8 offset:3744
	ds_read_b64 v[116:117], v8 offset:4032
	ds_read_b64 v[114:115], v8 offset:5184
	ds_read_b64 v[112:113], v8 offset:5472
	ds_read_b64 v[90:91], v8 offset:5760
	ds_read_b32 v43, v2
	ds_read_b32 v19, v2 offset:288
	ds_read_b32 v39, v2 offset:576
	ds_read_b32 v25, v2 offset:1728
	ds_read_b32 v7, v2 offset:2016
	ds_read_b32 v21, v2 offset:2304
	ds_read_b32 v11, v2 offset:3456
	ds_read_b32 v35, v2 offset:3744
	ds_read_b32 v59, v2 offset:4032
	ds_read_b32 v57, v2 offset:5184
	ds_read_b32 v51, v2 offset:5472
	ds_read_b32 v49, v2 offset:5760
	s_waitcnt lgkmcnt(0)
	v_mov_b32_e32 v64, v32
	v_mov_b32_e32 v46, v43
	v_mov_b32_e32 v65, v61
	v_mov_b64_e32 v[100:101], v[22:23]
	v_mov_b32_dpp v46, v61 row_shr:1 row_mask:0xf bank_mask:0xf
	v_pk_mul_f32 v[86:87], v[64:65], v[46:47]
	v_mov_b32_e32 v26, v19
	v_mov_b32_dpp v43, v60 row_shl:1 row_mask:0xf bank_mask:0xf
	v_pk_fma_f32 v[86:87], v[60:61], v[88:89], v[86:87] op_sel_hi:[0,1,1]
	v_pk_mov_b32 v[60:61], v[60:61], v[100:101] op_sel:[1,0]
	v_mov_b32_dpp v26, v63 row_shr:1 row_mask:0xf bank_mask:0xf
	v_mov_b32_e32 v1, v63
	v_accvgpr_read_b32 v67, a35
	v_pk_fma_f32 v[60:61], v[60:61], v[42:43], v[86:87]
	v_pk_mul_f32 v[86:87], v[0:1], v[26:27]
	v_accvgpr_read_b32 v66, a34
	v_accvgpr_write_b32 a10, v14
	v_mov_b32_dpp v19, v62 row_shl:1 row_mask:0xf bank_mask:0xf
	v_pk_fma_f32 v[86:87], v[62:63], v[16:17], v[86:87] op_sel_hi:[0,1,1]
	v_pk_mov_b32 v[62:63], v[62:63], v[66:67] op_sel:[1,0]
	v_mov_b32_e32 v44, v39
	v_accvgpr_write_b32 a11, v15
	v_pk_fma_f32 v[62:63], v[62:63], v[18:19], v[86:87]
	v_pk_add_f32 v[60:61], v[60:61], 0 op_sel_hi:[1,0]
	v_mov_b32_dpp v44, v69 row_shr:1 row_mask:0xf bank_mask:0xf
	v_mov_b32_e32 v31, v69
	v_accvgpr_read_b32 v14, a16
	v_accvgpr_read_b32 v28, a46
	v_pk_add_f32 v[60:61], v[60:61], v[62:63]
	v_pk_mul_f32 v[62:63], v[30:31], v[44:45]
	v_accvgpr_read_b32 v15, a17
	v_accvgpr_read_b32 v29, a47
	v_mov_b32_dpp v39, v68 row_shl:1 row_mask:0xf bank_mask:0xf
	v_pk_fma_f32 v[62:63], v[68:69], v[14:15], v[62:63] op_sel_hi:[0,1,1]
	v_pk_mov_b32 v[68:69], v[68:69], v[28:29] op_sel:[1,0]
	v_mov_b32_e32 v36, v25
	v_pk_fma_f32 v[62:63], v[68:69], v[38:39], v[62:63]
	s_mov_b64 s[0:1], 0x1400000
	v_pk_add_f32 v[60:61], v[60:61], v[62:63]
	v_mov_b32_dpp v36, v71 row_shr:1 row_mask:0xf bank_mask:0xf
	v_mov_b32_e32 v127, v71
	v_accvgpr_read_b32 v8, a20
	v_lshl_add_u64 v[62:63], v[54:55], 0, s[0:1]
	v_mov_b32_e32 v128, v60
	v_mov_b32_e32 v129, v61
	v_pk_mul_f32 v[60:61], v[126:127], v[36:37]
	v_accvgpr_read_b32 v9, a21
	v_accvgpr_write_b32 a25, v23
	v_mov_b32_e32 v12, v7
	v_mov_b32_dpp v25, v70 row_shl:1 row_mask:0xf bank_mask:0xf
	v_pk_fma_f32 v[60:61], v[70:71], v[8:9], v[60:61] op_sel_hi:[0,1,1]
	v_mov_b32_e32 v62, v71
	v_mov_b32_e32 v63, v101
	v_accvgpr_write_b32 a24, v22
	v_mov_b32_dpp v12, v73 row_shr:1 row_mask:0xf bank_mask:0xf
	v_mov_b32_e32 v74, v52
	v_mov_b32_e32 v75, v73
	v_accvgpr_read_b32 v23, a9
	v_accvgpr_write_b32 a26, v124
	v_accvgpr_mov_b32 a2, a22
	v_pk_fma_f32 v[60:61], v[62:63], v[24:25], v[60:61]
	v_pk_mul_f32 v[62:63], v[74:75], v[12:13]
	v_accvgpr_read_b32 v22, a8
	v_accvgpr_write_b32 a27, v125
	v_accvgpr_mov_b32 a3, a23
	v_accvgpr_write_b32 a22, v88
	v_mov_b32_dpp v7, v72 row_shl:1 row_mask:0xf bank_mask:0xf
	v_pk_fma_f32 v[62:63], v[72:73], v[22:23], v[62:63] op_sel_hi:[0,1,1]
	v_mov_b32_e32 v68, v73
	v_mov_b32_e32 v69, v67
	v_mov_b32_e32 v78, v21
	v_accvgpr_write_b32 a23, v89
	v_pk_fma_f32 v[62:63], v[68:69], v[6:7], v[62:63]
	v_pk_add_f32 v[60:61], v[60:61], 0 op_sel_hi:[1,0]
	v_mov_b32_dpp v78, v83 row_shr:1 row_mask:0xf bank_mask:0xf
	v_accvgpr_read_b32 v52, a30
	v_mov_b32_e32 v53, v83
	v_accvgpr_read_b32 v89, a27
	v_pk_add_f32 v[60:61], v[60:61], v[62:63]
	v_pk_mul_f32 v[62:63], v[52:53], v[78:79]
	v_accvgpr_read_b32 v88, a26
	v_mov_b32_dpp v21, v82 row_shl:1 row_mask:0xf bank_mask:0xf
	v_pk_fma_f32 v[62:63], v[82:83], v[88:89], v[62:63] op_sel_hi:[0,1,1]
	v_mov_b32_e32 v68, v83
	v_mov_b32_e32 v69, v29
	v_pk_fma_f32 v[62:63], v[68:69], v[20:21], v[62:63]
	v_mov_b32_e32 v76, v11
	v_accvgpr_read_b32 v125, a37
	v_pk_add_f32 v[60:61], v[60:61], v[62:63]
	s_mov_b64 s[0:1], 0x1410000
	v_mov_b32_dpp v76, v81 row_shr:1 row_mask:0xf bank_mask:0xf
	v_mov_b32_e32 v121, v81
	v_accvgpr_read_b32 v101, a15
	v_accvgpr_read_b32 v124, a36
	v_lshl_add_u64 v[136:137], v[134:135], 0, s[0:1]
	s_nop 1
	s_mov_b64 vcc, s[28:29]
	s_nop 0
	v_cndmask_b32_dpp v130, v60, v128, vcc quad_perm:[1,0,3,2] row_mask:0xf bank_mask:0xf
	v_cndmask_b32_dpp v131, v61, v129, vcc quad_perm:[1,0,3,2] row_mask:0xf bank_mask:0xf
	s_mov_b64 vcc, s[30:31]
	s_nop 0
	v_cndmask_b32_dpp v132, v128, v60, vcc quad_perm:[1,0,3,2] row_mask:0xf bank_mask:0xf
	v_cndmask_b32_dpp v133, v129, v61, vcc quad_perm:[1,0,3,2] row_mask:0xf bank_mask:0xf
	global_store_dwordx4 v[136:137], v[130:133], off sc0 sc1 nt
	s_nop 1
	v_pk_mul_f32 v[60:61], v[120:121], v[76:77]
	v_accvgpr_read_b32 v100, a14
	v_mov_b32_e32 v2, v35
	v_mov_b32_dpp v11, v80 row_shl:1 row_mask:0xf bank_mask:0xf
	v_pk_fma_f32 v[60:61], v[80:81], v[124:125], v[60:61] op_sel_hi:[0,1,1]
	v_pk_mov_b32 v[62:63], v[80:81], v[100:101] op_sel:[1,0]
	v_mov_b32_dpp v2, v85 row_shr:1 row_mask:0xf bank_mask:0xf
	v_mov_b32_e32 v107, v85
	v_accvgpr_read_b32 v29, a13
	v_pk_fma_f32 v[60:61], v[62:63], v[10:11], v[60:61]
	v_pk_mul_f32 v[62:63], v[106:107], v[2:3]
	v_accvgpr_read_b32 v28, a12
	v_mov_b32_dpp v35, v84 row_shl:1 row_mask:0xf bank_mask:0xf
	v_pk_fma_f32 v[62:63], v[84:85], v[28:29], v[62:63] op_sel_hi:[0,1,1]
	v_pk_mov_b32 v[68:69], v[84:85], v[122:123] op_sel:[1,0]
	v_mov_b32_e32 v92, v59
	v_pk_fma_f32 v[62:63], v[68:69], v[34:35], v[62:63]
	v_pk_add_f32 v[60:61], v[60:61], 0 op_sel_hi:[1,0]
	v_mov_b32_dpp v92, v117 row_shr:1 row_mask:0xf bank_mask:0xf
	v_mov_b32_e32 v97, v117
	v_pk_add_f32 v[60:61], v[60:61], v[62:63]
	v_pk_mul_f32 v[62:63], v[96:97], v[92:93]
	v_accvgpr_write_b32 a8, v118
	v_pk_fma_f32 v[62:63], v[116:117], v[118:119], v[62:63] op_sel_hi:[0,1,1]
	v_accvgpr_write_b32 a9, v119
	v_accvgpr_read_b32 v119, a45
	v_accvgpr_read_b32 v118, a44
	v_mov_b32_dpp v59, v116 row_shl:1 row_mask:0xf bank_mask:0xf
	v_pk_mov_b32 v[68:69], v[116:117], v[118:119] op_sel:[1,0]
	v_mov_b32_e32 v94, v57
	v_pk_fma_f32 v[62:63], v[68:69], v[58:59], v[62:63]
	s_mov_b64 s[0:1], 0x1420000
	v_pk_add_f32 v[60:61], v[60:61], v[62:63]
	v_mov_b32_dpp v94, v115 row_shr:1 row_mask:0xf bank_mask:0xf
	v_mov_b32_e32 v99, v115
	v_accvgpr_read_b32 v41, a11
	v_lshl_add_u64 v[62:63], v[54:55], 0, s[0:1]
	v_mov_b32_e32 v128, v60
	v_mov_b32_e32 v129, v61
	v_pk_mul_f32 v[60:61], v[98:99], v[94:95]
	v_accvgpr_read_b32 v40, a10
	v_mov_b32_e32 v102, v51
	v_mov_b32_dpp v57, v114 row_shl:1 row_mask:0xf bank_mask:0xf
	v_pk_fma_f32 v[60:61], v[114:115], v[40:41], v[60:61] op_sel_hi:[0,1,1]
	v_mov_b32_e32 v62, v115
	v_mov_b32_e32 v63, v101
	v_mov_b32_dpp v102, v113 row_shr:1 row_mask:0xf bank_mask:0xf
	v_mov_b32_e32 v105, v113
	v_pk_fma_f32 v[60:61], v[62:63], v[56:57], v[60:61]
	v_pk_mul_f32 v[62:63], v[104:105], v[102:103]
	v_mov_b32_dpp v51, v112 row_shl:1 row_mask:0xf bank_mask:0xf
	v_pk_fma_f32 v[62:63], v[112:113], v[4:5], v[62:63] op_sel_hi:[0,1,1]
	v_mov_b32_e32 v68, v113
	v_mov_b32_e32 v69, v123
	v_mov_b32_e32 v108, v49
	v_pk_fma_f32 v[62:63], v[68:69], v[50:51], v[62:63]
	v_pk_add_f32 v[60:61], v[60:61], 0 op_sel_hi:[1,0]
	v_mov_b32_dpp v108, v91 row_shr:1 row_mask:0xf bank_mask:0xf
	v_mov_b32_e32 v111, v91
	v_accvgpr_read_b32 v5, a3
	v_pk_add_f32 v[60:61], v[60:61], v[62:63]
	v_pk_mul_f32 v[62:63], v[110:111], v[108:109]
	v_accvgpr_read_b32 v4, a2
	v_mov_b32_dpp v49, v90 row_shl:1 row_mask:0xf bank_mask:0xf
	v_pk_fma_f32 v[62:63], v[90:91], v[4:5], v[62:63] op_sel_hi:[0,1,1]
	v_mov_b32_e32 v68, v91
	v_mov_b32_e32 v69, v119
	v_pk_fma_f32 v[62:63], v[68:69], v[48:49], v[62:63]
	s_mov_b64 s[0:1], 0x1430000
	v_pk_add_f32 v[60:61], v[60:61], v[62:63]
	v_lshl_add_u64 v[136:137], v[134:135], 0, s[0:1]
	s_nop 1
	s_mov_b64 vcc, s[28:29]
	s_nop 0
	v_cndmask_b32_dpp v130, v60, v128, vcc quad_perm:[1,0,3,2] row_mask:0xf bank_mask:0xf
	v_cndmask_b32_dpp v131, v61, v129, vcc quad_perm:[1,0,3,2] row_mask:0xf bank_mask:0xf
	s_mov_b64 vcc, s[30:31]
	s_nop 0
	v_cndmask_b32_dpp v132, v128, v60, vcc quad_perm:[1,0,3,2] row_mask:0xf bank_mask:0xf
	v_cndmask_b32_dpp v133, v129, v61, vcc quad_perm:[1,0,3,2] row_mask:0xf bank_mask:0xf
	global_store_dwordx4 v[136:137], v[130:133], off sc0 sc1 nt
	s_nop 1
	s_waitcnt vmcnt(12)
	s_waitcnt lgkmcnt(0)
	s_barrier
	v_accvgpr_read_b32 v2, a1
	v_accvgpr_read_b32 v12, a5
	ds_read_b64 v[60:61], v12
	ds_read_b64 v[62:63], v12 offset:288
	ds_read_b64 v[68:69], v12 offset:576
	ds_read_b64 v[70:71], v12 offset:1728
	ds_read_b64 v[72:73], v12 offset:2016
	ds_read_b64 v[82:83], v12 offset:2304
	ds_read_b64 v[80:81], v12 offset:3456
	ds_read_b64 v[84:85], v12 offset:3744
	ds_read_b64 v[116:117], v12 offset:4032
	ds_read_b64 v[114:115], v12 offset:5184
	ds_read_b64 v[112:113], v12 offset:5472
	ds_read_b64 v[90:91], v12 offset:5760
	ds_read_b32 v43, v2
	ds_read_b32 v19, v2 offset:288
	ds_read_b32 v39, v2 offset:576
	ds_read_b32 v25, v2 offset:1728
	ds_read_b32 v7, v2 offset:2016
	ds_read_b32 v21, v2 offset:2304
	ds_read_b32 v11, v2 offset:3456
	ds_read_b32 v35, v2 offset:3744
	ds_read_b32 v59, v2 offset:4032
	ds_read_b32 v57, v2 offset:5184
	ds_read_b32 v51, v2 offset:5472
	ds_read_b32 v49, v2 offset:5760
	s_waitcnt lgkmcnt(0)
	v_accvgpr_read_b32 v101, a23
	v_mov_b32_e32 v46, v43
	v_mov_b32_e32 v65, v61
	v_accvgpr_read_b32 v31, a25
	v_mov_b32_dpp v46, v61 row_shr:1 row_mask:0xf bank_mask:0xf
	v_pk_mul_f32 v[86:87], v[64:65], v[46:47]
	v_accvgpr_read_b32 v100, a22
	v_accvgpr_read_b32 v30, a24
	v_mov_b32_e32 v26, v19
	v_mov_b32_dpp v43, v60 row_shl:1 row_mask:0xf bank_mask:0xf
	v_pk_fma_f32 v[86:87], v[60:61], v[100:101], v[86:87] op_sel_hi:[0,1,1]
	v_pk_mov_b32 v[60:61], v[60:61], v[30:31] op_sel:[1,0]
	v_mov_b32_dpp v26, v63 row_shr:1 row_mask:0xf bank_mask:0xf
	v_mov_b32_e32 v1, v63
	v_pk_fma_f32 v[60:61], v[60:61], v[42:43], v[86:87]
	v_pk_mul_f32 v[86:87], v[0:1], v[26:27]
	v_accvgpr_read_b32 v0, a34
	v_accvgpr_mov_b32 a12, a14
	v_accvgpr_read_b32 v1, a35
	v_accvgpr_mov_b32 a13, a15
	v_mov_b32_dpp v19, v62 row_shl:1 row_mask:0xf bank_mask:0xf
	v_pk_fma_f32 v[86:87], v[62:63], v[16:17], v[86:87] op_sel_hi:[0,1,1]
	v_accvgpr_write_b32 a14, v16
	v_pk_mov_b32 v[62:63], v[62:63], v[0:1] op_sel:[1,0]
	v_mov_b32_e32 v44, v39
	v_accvgpr_write_b32 a15, v17
	v_pk_fma_f32 v[62:63], v[62:63], v[18:19], v[86:87]
	v_pk_add_f32 v[60:61], v[60:61], 0 op_sel_hi:[1,0]
	v_mov_b32_dpp v44, v69 row_shr:1 row_mask:0xf bank_mask:0xf
	v_accvgpr_read_b32 v16, a48
	v_mov_b32_e32 v17, v69
	v_accvgpr_read_b32 v67, a47
	v_pk_add_f32 v[60:61], v[60:61], v[62:63]
	v_pk_mul_f32 v[62:63], v[16:17], v[44:45]
	v_accvgpr_read_b32 v66, a46
	v_mov_b32_dpp v39, v68 row_shl:1 row_mask:0xf bank_mask:0xf
	v_pk_fma_f32 v[62:63], v[68:69], v[14:15], v[62:63] op_sel_hi:[0,1,1]
	v_pk_mov_b32 v[68:69], v[68:69], v[66:67] op_sel:[1,0]
	v_mov_b32_e32 v36, v25
	v_pk_fma_f32 v[62:63], v[68:69], v[38:39], v[62:63]
	s_mov_b64 s[0:1], 0x1800000
	v_pk_add_f32 v[60:61], v[60:61], v[62:63]
	v_mov_b32_dpp v36, v71 row_shr:1 row_mask:0xf bank_mask:0xf
	v_mov_b32_e32 v127, v71
	v_lshl_add_u64 v[62:63], v[54:55], 0, s[0:1]
	v_mov_b32_e32 v128, v60
	v_mov_b32_e32 v129, v61
	v_pk_mul_f32 v[60:61], v[126:127], v[36:37]
	v_mov_b32_e32 v12, v7
	v_mov_b32_dpp v25, v70 row_shl:1 row_mask:0xf bank_mask:0xf
	v_pk_fma_f32 v[60:61], v[70:71], v[8:9], v[60:61] op_sel_hi:[0,1,1]
	v_mov_b32_e32 v62, v71
	v_mov_b32_e32 v63, v31
	v_mov_b32_dpp v12, v73 row_shr:1 row_mask:0xf bank_mask:0xf
	v_mov_b32_e32 v75, v73
	v_pk_fma_f32 v[60:61], v[62:63], v[24:25], v[60:61]
	v_pk_mul_f32 v[62:63], v[74:75], v[12:13]
	v_mov_b32_dpp v7, v72 row_shl:1 row_mask:0xf bank_mask:0xf
	v_pk_fma_f32 v[62:63], v[72:73], v[22:23], v[62:63] op_sel_hi:[0,1,1]
	v_accvgpr_write_b32 a4, v22
	v_mov_b32_e32 v68, v73
	v_mov_b32_e32 v69, v1
	v_mov_b32_e32 v78, v21
	v_accvgpr_write_b32 a5, v23
	v_pk_fma_f32 v[62:63], v[68:69], v[6:7], v[62:63]
	v_pk_add_f32 v[60:61], v[60:61], 0 op_sel_hi:[1,0]
	v_mov_b32_dpp v78, v83 row_shr:1 row_mask:0xf bank_mask:0xf
	v_mov_b32_e32 v53, v83
	v_accvgpr_read_b32 v22, a26
	v_pk_add_f32 v[60:61], v[60:61], v[62:63]
	v_pk_mul_f32 v[62:63], v[52:53], v[78:79]
	v_accvgpr_read_b32 v23, a27
	v_mov_b32_dpp v21, v82 row_shl:1 row_mask:0xf bank_mask:0xf
	v_pk_fma_f32 v[62:63], v[82:83], v[22:23], v[62:63] op_sel_hi:[0,1,1]
	v_mov_b32_e32 v68, v83
	v_mov_b32_e32 v69, v67
	v_pk_fma_f32 v[62:63], v[68:69], v[20:21], v[62:63]
	v_mov_b32_e32 v76, v11
	v_pk_add_f32 v[60:61], v[60:61], v[62:63]
	s_mov_b64 s[0:1], 0x1810000
	v_mov_b32_dpp v76, v81 row_shr:1 row_mask:0xf bank_mask:0xf
	v_mov_b32_e32 v121, v81
	v_accvgpr_read_b32 v15, a13
	v_lshl_add_u64 v[136:137], v[134:135], 0, s[0:1]
	s_nop 1
	s_mov_b64 vcc, s[28:29]
	s_nop 0
	v_cndmask_b32_dpp v130, v60, v128, vcc quad_perm:[1,0,3,2] row_mask:0xf bank_mask:0xf
	v_cndmask_b32_dpp v131, v61, v129, vcc quad_perm:[1,0,3,2] row_mask:0xf bank_mask:0xf
	s_mov_b64 vcc, s[30:31]
	s_nop 0
	v_cndmask_b32_dpp v132, v128, v60, vcc quad_perm:[1,0,3,2] row_mask:0xf bank_mask:0xf
	v_cndmask_b32_dpp v133, v129, v61, vcc quad_perm:[1,0,3,2] row_mask:0xf bank_mask:0xf
	global_store_dwordx4 v[136:137], v[130:133], off sc0 sc1 nt
	s_nop 1
	v_pk_mul_f32 v[60:61], v[120:121], v[76:77]
	v_accvgpr_read_b32 v14, a12
	v_mov_b32_e32 v2, v35
	v_mov_b32_dpp v11, v80 row_shl:1 row_mask:0xf bank_mask:0xf
	v_pk_fma_f32 v[60:61], v[80:81], v[124:125], v[60:61] op_sel_hi:[0,1,1]
	v_pk_mov_b32 v[62:63], v[80:81], v[14:15] op_sel:[1,0]
	v_mov_b32_dpp v2, v85 row_shr:1 row_mask:0xf bank_mask:0xf
	v_mov_b32_e32 v107, v85
	v_pk_fma_f32 v[60:61], v[62:63], v[10:11], v[60:61]
	v_pk_mul_f32 v[62:63], v[106:107], v[2:3]
	v_mov_b32_dpp v35, v84 row_shl:1 row_mask:0xf bank_mask:0xf
	v_pk_fma_f32 v[62:63], v[84:85], v[28:29], v[62:63] op_sel_hi:[0,1,1]
	v_pk_mov_b32 v[68:69], v[84:85], v[122:123] op_sel:[1,0]
	v_mov_b32_e32 v92, v59
	v_pk_fma_f32 v[62:63], v[68:69], v[34:35], v[62:63]
	v_pk_add_f32 v[60:61], v[60:61], 0 op_sel_hi:[1,0]
	v_mov_b32_dpp v92, v117 row_shr:1 row_mask:0xf bank_mask:0xf
	v_mov_b32_e32 v97, v117
	v_accvgpr_read_b32 v87, a9
	v_pk_add_f32 v[60:61], v[60:61], v[62:63]
	v_pk_mul_f32 v[62:63], v[96:97], v[92:93]
	v_accvgpr_read_b32 v86, a8
	v_mov_b32_dpp v59, v116 row_shl:1 row_mask:0xf bank_mask:0xf
	v_pk_fma_f32 v[62:63], v[116:117], v[86:87], v[62:63] op_sel_hi:[0,1,1]
	v_pk_mov_b32 v[68:69], v[116:117], v[118:119] op_sel:[1,0]
	v_mov_b32_e32 v94, v57
	v_pk_fma_f32 v[62:63], v[68:69], v[58:59], v[62:63]
	s_mov_b64 s[0:1], 0x1820000
	v_pk_add_f32 v[60:61], v[60:61], v[62:63]
	v_mov_b32_dpp v94, v115 row_shr:1 row_mask:0xf bank_mask:0xf
	v_mov_b32_e32 v99, v115
	v_lshl_add_u64 v[62:63], v[54:55], 0, s[0:1]
	v_mov_b32_e32 v128, v60
	v_mov_b32_e32 v129, v61
	v_pk_mul_f32 v[60:61], v[98:99], v[94:95]
	v_mov_b32_e32 v102, v51
	v_mov_b32_dpp v57, v114 row_shl:1 row_mask:0xf bank_mask:0xf
	v_pk_fma_f32 v[60:61], v[114:115], v[40:41], v[60:61] op_sel_hi:[0,1,1]
	v_mov_b32_e32 v62, v115
	v_mov_b32_e32 v63, v15
	v_mov_b32_dpp v102, v113 row_shr:1 row_mask:0xf bank_mask:0xf
	v_mov_b32_e32 v105, v113
	v_accvgpr_read_b32 v89, a19
	v_pk_fma_f32 v[60:61], v[62:63], v[56:57], v[60:61]
	v_pk_mul_f32 v[62:63], v[104:105], v[102:103]
	v_accvgpr_read_b32 v88, a18
	v_mov_b32_dpp v51, v112 row_shl:1 row_mask:0xf bank_mask:0xf
	v_pk_fma_f32 v[62:63], v[112:113], v[88:89], v[62:63] op_sel_hi:[0,1,1]
	v_mov_b32_e32 v68, v113
	v_mov_b32_e32 v69, v123
	v_mov_b32_e32 v108, v49
	v_pk_fma_f32 v[62:63], v[68:69], v[50:51], v[62:63]
	v_pk_add_f32 v[60:61], v[60:61], 0 op_sel_hi:[1,0]
	v_mov_b32_dpp v108, v91 row_shr:1 row_mask:0xf bank_mask:0xf
	v_mov_b32_e32 v111, v91
	v_pk_add_f32 v[60:61], v[60:61], v[62:63]
	v_pk_mul_f32 v[62:63], v[110:111], v[108:109]
	v_mov_b32_dpp v49, v90 row_shl:1 row_mask:0xf bank_mask:0xf
	v_pk_fma_f32 v[62:63], v[90:91], v[4:5], v[62:63] op_sel_hi:[0,1,1]
	v_mov_b32_e32 v68, v91
	v_mov_b32_e32 v69, v119
	v_pk_fma_f32 v[62:63], v[68:69], v[48:49], v[62:63]
	s_mov_b64 s[0:1], 0x1830000
	v_pk_add_f32 v[60:61], v[60:61], v[62:63]
	v_lshl_add_u64 v[136:137], v[134:135], 0, s[0:1]
	s_nop 1
	s_mov_b64 vcc, s[28:29]
	s_nop 0
	v_cndmask_b32_dpp v130, v60, v128, vcc quad_perm:[1,0,3,2] row_mask:0xf bank_mask:0xf
	v_cndmask_b32_dpp v131, v61, v129, vcc quad_perm:[1,0,3,2] row_mask:0xf bank_mask:0xf
	s_mov_b64 vcc, s[30:31]
	s_nop 0
	v_cndmask_b32_dpp v132, v128, v60, vcc quad_perm:[1,0,3,2] row_mask:0xf bank_mask:0xf
	v_cndmask_b32_dpp v133, v129, v61, vcc quad_perm:[1,0,3,2] row_mask:0xf bank_mask:0xf
	global_store_dwordx4 v[136:137], v[130:133], off sc0 sc1 nt
	s_nop 1
	v_accvgpr_write_b32 a12, v28
	s_waitcnt vmcnt(8)
	v_accvgpr_write_b32 a13, v29
	v_mov_b64_e32 v[28:29], v[4:5]
	s_waitcnt lgkmcnt(0)
	s_barrier
	v_accvgpr_read_b32 v2, a6
	v_accvgpr_read_b32 v4, a7
	ds_read_b64 v[60:61], v2
	ds_read_b64 v[62:63], v2 offset:288
	ds_read_b64 v[68:69], v2 offset:576
	ds_read_b64 v[70:71], v2 offset:1728
	ds_read_b64 v[72:73], v2 offset:2016
	ds_read_b64 v[82:83], v2 offset:2304
	ds_read_b64 v[80:81], v2 offset:3456
	ds_read_b64 v[84:85], v2 offset:3744
	ds_read_b64 v[116:117], v2 offset:4032
	ds_read_b64 v[114:115], v2 offset:5184
	ds_read_b64 v[112:113], v2 offset:5472
	ds_read_b64 v[90:91], v2 offset:5760
	ds_read_b32 v43, v4
	ds_read_b32 v19, v4 offset:288
	ds_read_b32 v39, v4 offset:576
	ds_read_b32 v25, v4 offset:1728
	ds_read_b32 v7, v4 offset:2016
	ds_read_b32 v21, v4 offset:2304
	ds_read_b32 v11, v4 offset:3456
	ds_read_b32 v35, v4 offset:3744
	ds_read_b32 v59, v4 offset:4032
	ds_read_b32 v57, v4 offset:5184
	ds_read_b32 v51, v4 offset:5472
	ds_read_b32 v49, v4 offset:5760
	s_waitcnt lgkmcnt(0)
	v_accvgpr_read_b32 v8, a24
	v_mov_b32_e32 v46, v43
	v_mov_b32_e32 v65, v61
	v_mov_b32_e32 v26, v19
	v_mov_b32_dpp v46, v61 row_shr:1 row_mask:0xf bank_mask:0xf
	v_accvgpr_read_b32 v32, a32
	v_accvgpr_read_b32 v9, a25
	v_mov_b64_e32 v[124:125], v[40:41]
	v_pk_mul_f32 v[30:31], v[64:65], v[46:47]
	v_mov_b32_dpp v26, v63 row_shr:1 row_mask:0xf bank_mask:0xf
	v_mov_b32_e32 v33, v63
	v_accvgpr_read_b32 v4, a14
	v_accvgpr_read_b32 v41, a35
	v_mov_b32_e32 v44, v39
	v_pk_fma_f32 v[30:31], v[60:61], v[100:101], v[30:31] op_sel_hi:[0,1,1]
	v_mov_b32_dpp v43, v60 row_shl:1 row_mask:0xf bank_mask:0xf
	v_pk_mov_b32 v[46:47], v[60:61], v[8:9] op_sel:[1,0]
	v_pk_mul_f32 v[26:27], v[32:33], v[26:27]
	v_accvgpr_read_b32 v5, a15
	v_accvgpr_read_b32 v40, a34
	v_mov_b32_dpp v44, v69 row_shr:1 row_mask:0xf bank_mask:0xf
	v_mov_b32_e32 v17, v69
	v_accvgpr_read_b32 v0, a16
	v_pk_fma_f32 v[30:31], v[46:47], v[42:43], v[30:31]
	v_pk_fma_f32 v[26:27], v[62:63], v[4:5], v[26:27] op_sel_hi:[0,1,1]
	v_mov_b32_dpp v19, v62 row_shl:1 row_mask:0xf bank_mask:0xf
	v_pk_mov_b32 v[32:33], v[62:63], v[40:41] op_sel:[1,0]
	v_pk_mul_f32 v[16:17], v[16:17], v[44:45]
	v_accvgpr_read_b32 v1, a17
	v_pk_fma_f32 v[18:19], v[32:33], v[18:19], v[26:27]
	v_pk_add_f32 v[26:27], v[30:31], 0 op_sel_hi:[1,0]
	v_mov_b32_dpp v39, v68 row_shl:1 row_mask:0xf bank_mask:0xf
	v_pk_fma_f32 v[16:17], v[68:69], v[0:1], v[16:17] op_sel_hi:[0,1,1]
	v_pk_mov_b32 v[30:31], v[68:69], v[66:67] op_sel:[1,0]
	v_pk_add_f32 v[18:19], v[26:27], v[18:19]
	v_pk_fma_f32 v[16:17], v[30:31], v[38:39], v[16:17]
	v_mov_b32_e32 v36, v25
	s_mov_b64 s[0:1], 0x1c00000
	v_pk_add_f32 v[16:17], v[18:19], v[16:17]
	v_mov_b32_dpp v36, v71 row_shr:1 row_mask:0xf bank_mask:0xf
	v_mov_b32_e32 v127, v71
	v_accvgpr_read_b32 v0, a20
	v_lshl_add_u64 v[26:27], v[54:55], 0, s[0:1]
	v_mov_b32_e32 v128, v16
	v_mov_b32_e32 v129, v17
	v_mov_b32_e32 v12, v7
	v_pk_mul_f32 v[16:17], v[126:127], v[36:37]
	v_accvgpr_read_b32 v1, a21
	v_mov_b32_dpp v12, v73 row_shr:1 row_mask:0xf bank_mask:0xf
	v_pk_fma_f32 v[16:17], v[70:71], v[0:1], v[16:17] op_sel_hi:[0,1,1]
	v_mov_b32_e32 v75, v73
	v_accvgpr_read_b32 v0, a4
	v_mov_b32_e32 v78, v21
	v_pk_mul_f32 v[12:13], v[74:75], v[12:13]
	v_accvgpr_read_b32 v1, a5
	v_mov_b32_dpp v25, v70 row_shl:1 row_mask:0xf bank_mask:0xf
	v_mov_b32_dpp v7, v72 row_shl:1 row_mask:0xf bank_mask:0xf
	v_mov_b32_dpp v78, v83 row_shr:1 row_mask:0xf bank_mask:0xf
	v_mov_b32_e32 v8, v71
	v_pk_fma_f32 v[12:13], v[72:73], v[0:1], v[12:13] op_sel_hi:[0,1,1]
	v_mov_b32_e32 v5, v41
	v_mov_b32_e32 v4, v73
	v_mov_b32_e32 v53, v83
	v_pk_fma_f32 v[16:17], v[8:9], v[24:25], v[16:17]
	v_pk_fma_f32 v[6:7], v[4:5], v[6:7], v[12:13]
	v_pk_mul_f32 v[12:13], v[52:53], v[78:79]
	v_mov_b32_dpp v21, v82 row_shl:1 row_mask:0xf bank_mask:0xf
	v_pk_add_f32 v[16:17], v[16:17], 0 op_sel_hi:[1,0]
	v_pk_fma_f32 v[12:13], v[82:83], v[22:23], v[12:13] op_sel_hi:[0,1,1]
	v_mov_b32_e32 v66, v83
	v_pk_add_f32 v[6:7], v[16:17], v[6:7]
	v_pk_fma_f32 v[12:13], v[66:67], v[20:21], v[12:13]
	v_mov_b32_e32 v76, v11
	v_pk_add_f32 v[6:7], v[6:7], v[12:13]
	s_mov_b64 s[0:1], 0x1c10000
	v_mov_b32_dpp v76, v81 row_shr:1 row_mask:0xf bank_mask:0xf
	v_mov_b32_e32 v121, v81
	v_accvgpr_read_b32 v0, a36
	v_lshl_add_u64 v[136:137], v[134:135], 0, s[0:1]
	s_nop 1
	s_mov_b64 vcc, s[28:29]
	s_nop 0
	v_cndmask_b32_dpp v130, v6, v128, vcc quad_perm:[1,0,3,2] row_mask:0xf bank_mask:0xf
	v_cndmask_b32_dpp v131, v7, v129, vcc quad_perm:[1,0,3,2] row_mask:0xf bank_mask:0xf
	s_mov_b64 vcc, s[30:31]
	s_nop 0
	v_cndmask_b32_dpp v132, v128, v6, vcc quad_perm:[1,0,3,2] row_mask:0xf bank_mask:0xf
	v_cndmask_b32_dpp v133, v129, v7, vcc quad_perm:[1,0,3,2] row_mask:0xf bank_mask:0xf
	global_store_dwordx4 v[136:137], v[130:133], off sc0 sc1 nt
	s_nop 1
	v_mov_b32_e32 v2, v35
	v_pk_mul_f32 v[6:7], v[120:121], v[76:77]
	v_accvgpr_read_b32 v1, a37
	v_mov_b32_dpp v2, v85 row_shr:1 row_mask:0xf bank_mask:0xf
	v_pk_fma_f32 v[6:7], v[80:81], v[0:1], v[6:7] op_sel_hi:[0,1,1]
	v_mov_b32_e32 v107, v85
	v_accvgpr_read_b32 v0, a12
	v_mov_b32_e32 v92, v59
	v_pk_mul_f32 v[2:3], v[106:107], v[2:3]
	v_accvgpr_read_b32 v1, a13
	v_mov_b32_dpp v11, v80 row_shl:1 row_mask:0xf bank_mask:0xf
	v_mov_b32_dpp v35, v84 row_shl:1 row_mask:0xf bank_mask:0xf
	v_mov_b32_dpp v92, v117 row_shr:1 row_mask:0xf bank_mask:0xf
	v_pk_mov_b32 v[8:9], v[80:81], v[14:15] op_sel:[1,0]
	v_pk_fma_f32 v[2:3], v[84:85], v[0:1], v[2:3] op_sel_hi:[0,1,1]
	v_pk_mov_b32 v[4:5], v[84:85], v[122:123] op_sel:[1,0]
	v_mov_b32_e32 v97, v117
	v_pk_fma_f32 v[6:7], v[8:9], v[10:11], v[6:7]
	v_pk_fma_f32 v[0:1], v[4:5], v[34:35], v[2:3]
	v_pk_mul_f32 v[2:3], v[96:97], v[92:93]
	v_mov_b32_dpp v59, v116 row_shl:1 row_mask:0xf bank_mask:0xf
	v_pk_add_f32 v[6:7], v[6:7], 0 op_sel_hi:[1,0]
	v_pk_fma_f32 v[2:3], v[116:117], v[86:87], v[2:3] op_sel_hi:[0,1,1]
	v_pk_mov_b32 v[4:5], v[116:117], v[118:119] op_sel:[1,0]
	v_pk_add_f32 v[0:1], v[6:7], v[0:1]
	v_pk_fma_f32 v[2:3], v[4:5], v[58:59], v[2:3]
	v_mov_b32_e32 v94, v57
	v_pk_add_f32 v[0:1], v[0:1], v[2:3]
	s_mov_b64 s[0:1], 0x1c20000
	v_mov_b32_dpp v94, v115 row_shr:1 row_mask:0xf bank_mask:0xf
	v_mov_b32_e32 v102, v51
	v_mov_b32_e32 v99, v115
	v_lshl_add_u64 v[2:3], v[54:55], 0, s[0:1]
	v_mov_b32_e32 v128, v0
	v_mov_b32_e32 v129, v1
	v_mov_b32_dpp v102, v113 row_shr:1 row_mask:0xf bank_mask:0xf
	v_pk_mul_f32 v[0:1], v[98:99], v[94:95]
	v_mov_b32_e32 v105, v113
	v_mov_b32_dpp v57, v114 row_shl:1 row_mask:0xf bank_mask:0xf
	v_pk_fma_f32 v[0:1], v[114:115], v[124:125], v[0:1] op_sel_hi:[0,1,1]
	v_mov_b32_e32 v14, v115
	v_pk_mul_f32 v[2:3], v[104:105], v[102:103]
	v_mov_b32_dpp v51, v112 row_shl:1 row_mask:0xf bank_mask:0xf
	v_mov_b32_e32 v108, v49
	v_pk_fma_f32 v[0:1], v[14:15], v[56:57], v[0:1]
	v_pk_fma_f32 v[2:3], v[112:113], v[88:89], v[2:3] op_sel_hi:[0,1,1]
	v_mov_b32_e32 v122, v113
	v_mov_b32_dpp v108, v91 row_shr:1 row_mask:0xf bank_mask:0xf
	v_pk_add_f32 v[0:1], v[0:1], 0 op_sel_hi:[1,0]
	v_pk_fma_f32 v[2:3], v[122:123], v[50:51], v[2:3]
	v_mov_b32_e32 v111, v91
	v_pk_add_f32 v[0:1], v[0:1], v[2:3]
	v_pk_mul_f32 v[2:3], v[110:111], v[108:109]
	v_mov_b32_dpp v49, v90 row_shl:1 row_mask:0xf bank_mask:0xf
	v_pk_fma_f32 v[2:3], v[90:91], v[28:29], v[2:3] op_sel_hi:[0,1,1]
	v_mov_b32_e32 v118, v91
	v_pk_fma_f32 v[2:3], v[118:119], v[48:49], v[2:3]
	s_mov_b64 s[0:1], 0x1c30000
	v_pk_add_f32 v[0:1], v[0:1], v[2:3]
	v_lshl_add_u64 v[136:137], v[134:135], 0, s[0:1]
	s_nop 1
	s_mov_b64 vcc, s[28:29]
	s_nop 0
	v_cndmask_b32_dpp v130, v0, v128, vcc quad_perm:[1,0,3,2] row_mask:0xf bank_mask:0xf
	v_cndmask_b32_dpp v131, v1, v129, vcc quad_perm:[1,0,3,2] row_mask:0xf bank_mask:0xf
	s_mov_b64 vcc, s[30:31]
	s_nop 0
	v_cndmask_b32_dpp v132, v128, v0, vcc quad_perm:[1,0,3,2] row_mask:0xf bank_mask:0xf
	v_cndmask_b32_dpp v133, v129, v1, vcc quad_perm:[1,0,3,2] row_mask:0xf bank_mask:0xf
	global_store_dwordx4 v[136:137], v[130:133], off sc0 sc1 nt
	s_nop 1
	s_endpgm
